# attention latent loop unrolled x3 (6 key tiles per iteration): ring slots are compile-time constants, K/V fragment reads use loop-invariant address VGPRs + immediates, DMA destinations s84+constant; n
# speedup vs baseline: 1.0264x; 1.0048x over previous
.LBB0_783:
	s_and_b64 vcc, exec, s[0:1]
	s_cbranch_vccz .LBB0_762
	s_ashr_i32 s0, s16, 7
	s_lshl_b32 s18, s0, 11
	s_and_b32 s1, s17, 0x780
	s_or_b32 s17, s18, s1
	s_lshl_b32 s1, s16, 3
	s_and_b32 s1, s1, 0x380
	v_mbcnt_lo_u32_b32 v171, -1, 0
	v_mbcnt_hi_u32_b32 v171, -1, v171
	s_lshl_b32 s96, s1, 1
	v_lshlrev_b32_e32 v20, 3, v171
	v_and_b32_e32 v0, 0x78, v20
	s_add_u32 s20, s6, s96
	v_lshlrev_b32_e32 v16, 1, v0
	s_addc_u32 s21, s7, 0
	v_mov_b32_e32 v17, v113
	v_add_u32_e32 v172, s4, v171
	v_lshl_add_u64 v[166:167], s[20:21], 0, v[16:17]
	s_add_u32 s20, s8, s96
	v_ashrrev_i32_e32 v181, 4, v172
	s_addc_u32 s21, s9, 0
	v_lshl_add_u64 v[168:169], s[20:21], 0, v[16:17]
	v_mad_u32_u24 v241, v181, s62, v16
	v_add_u32_e32 v34, s18, v181
	v_mad_i64_i32 v[0:1], s[20:21], v34, s62, v[168:169]
	v_add_co_u32_e32 v4, vcc, s74, v0
	v_mad_i64_i32 v[8:9], s[20:21], v34, s62, v[166:167]
	s_nop 0
	v_addc_co_u32_e32 v5, vcc, 0, v1, vcc
	v_add_co_u32_e32 v12, vcc, s74, v8
	global_load_dwordx4 v[0:3], v[0:1], off
	s_nop 0
	global_load_dwordx4 v[4:7], v[4:5], off
	v_addc_co_u32_e32 v13, vcc, 0, v9, vcc
	global_load_dwordx4 v[8:11], v[8:9], off
	s_nop 0
	global_load_dwordx4 v[12:15], v[12:13], off
	v_lshrrev_b32_e32 v17, 1, v172
	v_and_b32_e32 v173, 31, v171
	v_and_b32_e32 v176, 0x60, v17
	v_mov_b64_e32 v[18:19], s[50:51]
	v_ashrrev_i32_e32 v175, 8, v172
	v_or3_b32 v29, v173, s17, v176
	v_bfe_u32 v22, v20, 5, 2
	v_lshlrev_b32_e32 v20, 6, v175
	v_mad_i64_i32 v[18:19], s[20:21], v29, s62, v[18:19]
	v_bfe_u32 v174, v171, 5, 1
	v_ashrrev_i32_e32 v21, 31, v20
	v_lshl_add_u64 v[18:19], v[18:19], 0, s[96:97]
	v_lshlrev_b32_e32 v112, 4, v174
	v_lshl_add_u64 v[18:19], v[20:21], 1, v[18:19]
	v_lshl_add_u64 v[18:19], v[18:19], 0, v[112:113]
	global_load_dwordx4 v[122:125], v[18:19], off
	global_load_dwordx4 v[126:129], v[18:19], off offset:32
	global_load_dwordx4 v[118:121], v[18:19], off offset:64
	global_load_dwordx4 v[114:117], v[18:19], off offset:96
	v_and_b32_e32 v17, 0xfffff0, v181
	v_lshlrev_b32_e32 v24, 1, v181
	v_add_u32_e32 v27, 32, v181
	v_lshrrev_b32_e32 v25, 1, v181
	v_and_b32_e32 v26, 3, v181
	v_and_or_b32 v17, v181, 8, v17
	v_and_b32_e32 v20, 0xfffff0, v27
	v_lshlrev_b32_e32 v21, 1, v27
	v_and_b32_e32 v23, 0x70, v172
	v_lshlrev_b32_e32 v28, 8, v181
	v_and_or_b32 v24, v181, 4, v26
	v_lshlrev_b32_e32 v26, 8, v27
	v_lshrrev_b32_e32 v17, 1, v17
	v_and_or_b32 v20, v27, 8, v20
	v_and_b32_e32 v25, 48, v16
	v_bitop3_b32 v182, v16, v28, v23 bitop3:0xde
	v_bitop3_b32 v183, v26, v16, v23 bitop3:0xf6
	v_and_b32_e32 v243, 16, v181
	v_lshlrev_b32_e32 v243, 3, v243
	v_xor_b32_e32 v182, v243, v182
	v_xor_b32_e32 v183, v243, v183
	v_or_b32_e32 v16, v17, v22
	v_lshrrev_b32_e32 v17, 1, v20
	v_lshlrev_b32_e32 v24, 6, v24
	v_lshlrev_b32_e32 v16, 9, v16
	v_or_b32_e32 v17, v17, v22
	v_or3_b32 v184, v16, v24, v25
	v_lshlrev_b32_e32 v16, 9, v17
	v_or3_b32 v185, v16, v24, v25
	v_add_u32_e32 v32, 0, v184
	v_add_u32_e32 v21, 0, v182
	v_add_u32_e32 v20, 0, v183
	v_add_u32_e32 v33, 0, v185
	s_waitcnt vmcnt(0)
	v_lshlrev_b32_e32 v38, 7, v175
	v_lshlrev_b32_e32 v189, 8, v173
	v_add_u32_e32 v191, 0, v189
	s_movk_i32 s1, 0x60
	s_waitcnt vmcnt(7)
	ds_write_b128 v32, v[0:3] offset:1024
	s_waitcnt vmcnt(6)
	ds_write_b128 v33, v[4:7] offset:1024
	s_waitcnt vmcnt(5)
	ds_write_b128 v21, v[8:11] offset:50176
	s_waitcnt vmcnt(4)
	ds_write_b128 v20, v[12:15] offset:50176
	v_add_u32_e32 v4, 64, v34
	v_mad_i64_i32 v[0:1], s[20:21], v4, s62, v[168:169]
	v_add_co_u32_e32 v2, vcc, s74, v0
	s_nop 1
	v_addc_co_u32_e32 v3, vcc, 0, v1, vcc
	global_load_dwordx4 v[16:19], v[0:1], off
	global_load_dwordx4 v[20:23], v[2:3], off
	v_mad_i64_i32 v[0:1], s[20:21], v4, s62, v[166:167]
	v_add_co_u32_e32 v2, vcc, s74, v0
	v_add_u32_e32 v4, 0x80, v34
	s_nop 0
	v_addc_co_u32_e32 v3, vcc, 0, v1, vcc
	global_load_dwordx4 v[24:27], v[0:1], off
	global_load_dwordx4 v[28:31], v[2:3], off
	v_mad_i64_i32 v[0:1], s[20:21], v4, s62, v[166:167]
	v_add_co_u32_e32 v2, vcc, s74, v0
	s_nop 1
	v_addc_co_u32_e32 v3, vcc, 0, v1, vcc
	v_mad_i64_i32 v[0:1], s[20:21], v4, s62, v[168:169]
	v_add_co_u32_e32 v2, vcc, s74, v0
	s_nop 1
	v_addc_co_u32_e32 v3, vcc, 0, v1, vcc
	v_lshlrev_b32_e32 v0, 4, v171
	v_and_b32_e32 v39, 0x70, v0
	v_bitop3_b32 v190, v38, v39, v112 bitop3:0x36
	v_and_b32_e32 v244, 16, v171
	v_lshlrev_b32_e32 v244, 3, v244
	v_xor_b32_e32 v190, v244, v190
	v_add_u32_e32 v34, v191, v190
	s_waitcnt lgkmcnt(0)
	s_barrier
	ds_read_b128 v[0:3], v34 offset:50176
	ds_read_b128 v[34:37], v34 offset:58368
	v_or_b32_e32 v38, v38, v112
	v_bitop3_b32 v188, v38, v39, 32 bitop3:0x36
	v_xor_b32_e32 v188, v244, v188
	v_add_u32_e32 v40, v191, v188
	s_waitcnt vmcnt(7) lgkmcnt(0)
	v_mfma_f32_32x32x16_bf16 v[64:79], v[34:37], v[122:125], 0
	ds_read_b128 v[34:37], v40 offset:50176
	v_bitop3_b32 v187, v38, v39, 64 bitop3:0x36
	v_bitop3_b32 v186, v38, v39, s1 bitop3:0x36
	v_xor_b32_e32 v187, v244, v187
	v_xor_b32_e32 v186, v244, v186
	v_add_u32_e32 v38, v191, v186
	v_mfma_f32_32x32x16_bf16 v[0:15], v[0:3], v[122:125], 0
	s_waitcnt vmcnt(6) lgkmcnt(0)
	v_mfma_f32_32x32x16_bf16 v[0:15], v[34:37], v[126:129], v[0:15]
	ds_read_b128 v[34:37], v40 offset:58368
	v_add_u32_e32 v40, v191, v187
	s_waitcnt lgkmcnt(0)
	v_mfma_f32_32x32x16_bf16 v[64:79], v[34:37], v[126:129], v[64:79]
	ds_read_b128 v[34:37], v40 offset:50176
	s_waitcnt vmcnt(5) lgkmcnt(0)
	v_mfma_f32_32x32x16_bf16 v[0:15], v[34:37], v[118:121], v[0:15]
	ds_read_b128 v[34:37], v40 offset:58368
	s_waitcnt lgkmcnt(0)
	v_mfma_f32_32x32x16_bf16 v[64:79], v[34:37], v[118:121], v[64:79]
	ds_read_b128 v[34:37], v38 offset:50176
	s_waitcnt vmcnt(4) lgkmcnt(0)
	v_mfma_f32_32x32x16_bf16 v[0:15], v[34:37], v[114:117], v[0:15]
	ds_read_b128 v[34:37], v38 offset:58368
	s_waitcnt lgkmcnt(0)
	v_mfma_f32_32x32x16_bf16 v[64:79], v[34:37], v[114:117], v[64:79]
	s_nop 8
	v_max_f32_e32 v34, v1, v1
	v_max_f32_e32 v35, v0, v0
	v_max_f32_e32 v34, v35, v34
	v_max3_f32 v34, v34, v2, v3
	v_max3_f32 v34, v34, v4, v5
	v_max3_f32 v34, v34, v6, v7
	v_max3_f32 v34, v34, v8, v9
	v_max3_f32 v34, v34, v10, v11
	v_max3_f32 v34, v34, v12, v13
	v_max3_f32 v34, v34, v14, v15
	v_max3_f32 v34, v34, v64, v65
	v_max3_f32 v34, v34, v66, v67
	v_max3_f32 v34, v34, v68, v69
	v_max3_f32 v34, v34, v70, v71
	v_max3_f32 v34, v34, v72, v73
	v_max3_f32 v34, v34, v74, v75
	v_max3_f32 v34, v34, v76, v77
	v_max3_f32 v34, v34, v78, v79
	v_mov_b32_e32 v35, v34
	s_nop 1
	v_permlane32_swap_b32_e32 v34, v35
	v_max_f32_e32 v35, v35, v35
	v_max_f32_e32 v34, v34, v34
	v_max_f32_e32 v34, v34, v35
	v_cmp_ge_f32_e32 vcc, s75, v34
	s_cmp_eq_u64 vcc, exec
	s_cbranch_scc0 .LBB0_814
	v_mov_b32_e32 v193, 1.0
	v_mov_b32_e32 v164, 0
	s_mov_b32 s56, s75
.LBB0_786:
	v_and_b32_e32 v34, 63, v171
	s_lshl_b32 s16, s0, 8
	v_and_b32_e32 v35, 0x3fffffc0, v172
	v_readlane_b32 s0, v254, 42
	v_lshlrev_b32_e32 v36, 4, v34
	v_and_b32_e32 v36, 0xc0, v36
	v_lshl_add_u32 v177, v35, 2, s0
	v_lshlrev_b32_e32 v35, 3, v34
	v_lshlrev_b32_e32 v37, 1, v34
	v_and_or_b32 v36, v35, 24, v36
	v_and_b32_e32 v37, 32, v37
	v_and_b32_e32 v35, 0x100, v35
	v_or3_b32 v192, v36, v37, v35
	s_add_i32 s1, 0, 0x400
	v_add_u32_e32 v194, s1, v192
	s_add_i32 s1, 0, 0x10400
	s_waitcnt vmcnt(0)
	s_waitcnt vmcnt(0)
	ds_write_b128 v32, v[16:19] offset:17408
	s_waitcnt vmcnt(0)
	ds_write_b128 v33, v[20:23] offset:17408
	v_add_u32_e32 v16, s1, v182
	v_exp_f32_e32 v159, v0
	v_exp_f32_e32 v161, v1
	v_exp_f32_e32 v157, v2
	v_exp_f32_e32 v160, v3
	v_exp_f32_e32 v155, v4
	v_exp_f32_e32 v158, v5
	v_exp_f32_e32 v154, v6
	v_exp_f32_e32 v156, v7
	v_exp_f32_e32 v151, v8
	v_exp_f32_e32 v153, v9
	v_exp_f32_e32 v149, v10
	v_exp_f32_e32 v152, v11
	v_exp_f32_e32 v147, v12
	v_exp_f32_e32 v150, v13
	v_exp_f32_e32 v146, v14
	v_exp_f32_e32 v148, v15
	s_waitcnt vmcnt(0)
	ds_write_b128 v16, v[24:27]
	v_add_u32_e32 v16, s1, v183
	v_mov_b32_e32 v14, v113
	v_mov_b32_e32 v15, v113
	s_waitcnt vmcnt(0)
	ds_write_b128 v16, v[28:31]
	v_cmp_gt_u32_e64 s[38:39], 32, v34
	v_mov_b32_e32 v0, v113
	v_mov_b32_e32 v1, v113
	v_mov_b32_e32 v2, v113
	v_mov_b32_e32 v3, v113
	v_mov_b32_e32 v4, v113
	v_mov_b32_e32 v5, v113
	v_mov_b32_e32 v6, v113
	v_mov_b32_e32 v7, v113
	v_mov_b32_e32 v8, v113
	v_mov_b32_e32 v9, v113
	v_mov_b32_e32 v10, v113
	v_mov_b32_e32 v11, v113
	v_mov_b32_e32 v12, v113
	v_mov_b32_e32 v13, v113
	v_mov_b64_e32 v[62:63], v[14:15]
	v_mov_b64_e32 v[46:47], v[14:15]
	v_mov_b64_e32 v[30:31], v[14:15]
	s_add_i32 s16, s16, 0x8000
	s_mov_b32 s19, 2
	s_mov_b32 s28, 4
	s_mov_b32 s0, 1
	v_lshl_add_u32 v178, v173, 2, v177
	s_mov_b32 s29, 0
	v_mov_b32_e32 v179, 0
	v_mov_b64_e32 v[60:61], v[12:13]
	v_mov_b64_e32 v[58:59], v[10:11]
	v_mov_b64_e32 v[56:57], v[8:9]
	v_mov_b64_e32 v[54:55], v[6:7]
	v_mov_b64_e32 v[52:53], v[4:5]
	v_mov_b64_e32 v[50:51], v[2:3]
	v_mov_b64_e32 v[48:49], v[0:1]
	v_mov_b64_e32 v[44:45], v[12:13]
	v_mov_b64_e32 v[42:43], v[10:11]
	v_mov_b64_e32 v[40:41], v[8:9]
	v_mov_b64_e32 v[38:39], v[6:7]
	v_mov_b64_e32 v[36:37], v[4:5]
	v_mov_b64_e32 v[34:35], v[2:3]
	v_mov_b64_e32 v[32:33], v[0:1]
	v_mov_b64_e32 v[28:29], v[12:13]
	v_mov_b64_e32 v[26:27], v[10:11]
	v_mov_b64_e32 v[24:25], v[8:9]
	v_mov_b64_e32 v[22:23], v[6:7]
	v_mov_b64_e32 v[20:21], v[4:5]
	v_mov_b64_e32 v[18:19], v[2:3]
	v_mov_b64_e32 v[16:17], v[0:1]
	s_waitcnt lgkmcnt(0)
	s_add_u32 s78, s8, s96
	s_addc_u32 s79, s9, 0
	s_add_u32 s80, s6, s96
	s_addc_u32 s81, s7, 0
	v_and_b32_e32 v183, 7, v181
	v_lshrrev_b32_e32 v185, 4, v181
	v_lshlrev_b32_e32 v185, 3, v185
	v_xor_b32_e32 v183, v183, v185
	v_and_b32_e32 v185, 15, v172
	v_xor_b32_e32 v183, v183, v185
	v_lshlrev_b32_e32 v183, 4, v183
	v_mad_u32_u24 v183, v181, s62, v183
	v_lshrrev_b32_e32 v185, 7, v172
	v_lshlrev_b32_e32 v185, 3, v185
	v_bfe_u32 v184, v172, 2, 3
	v_add_u32_e32 v185, v185, v184
	v_bfe_u32 v184, v172, 5, 2
	v_lshlrev_b32_e32 v184, 2, v184
	v_and_b32_e32 v182, 3, v172
	v_add_u32_e32 v184, v184, v182
	v_lshlrev_b32_e32 v184, 4, v184
	v_mad_u32_u24 v185, v185, s62, v184
	v_add_u32_e32 v182, 0x30000, v183
	v_add_u32_e32 v184, 0x30000, v185
	s_mul_i32 s89, s16, 0x1800
	s_mov_b32 s20, 0x8000
	v_add_u32_e32 v130, v191, v190
	v_add_u32_e32 v131, v191, v188
	v_add_u32_e32 v132, v191, v187
	v_add_u32_e32 v133, v191, v186
	v_add_u32_e32 v134, 0x8000, v130
	v_add_u32_e32 v135, 0x8000, v131
	v_add_u32_e32 v136, 0x8000, v132
	v_add_u32_e32 v137, 0x8000, v133
	s_mov_b32 s55, 1
	s_lshl_b32 s84, s90, 10
	s_add_i32 s65, s18, 0x80
	s_mul_i32 s65, s65, 0x1800
	s_add_u32 s66, s80, s65
	s_addc_u32 s67, s81, 0
	s_add_i32 s85, s84, 0x14400
	s_mov_b32 m0, s85
	s_nop 0
	global_load_lds_dwordx4 v183, s[66:67]
	s_add_i32 m0, s85, 0x2000
	s_nop 0
	global_load_lds_dwordx4 v182, s[66:67]
	s_barrier
.LBB0_787:
	ds_read_b128 v[80:83], v134 offset:33792
	ds_read_b128 v[84:87], v134 offset:41984
	ds_read_b128 v[196:199], v135 offset:33792
	ds_read_b128 v[200:203], v135 offset:41984
	s_waitcnt lgkmcnt(2)
	v_mfma_f32_32x32x16_bf16 v[96:111], v[80:83], v[122:125], 0
	v_exp_f32_e32 v204, v72
	v_exp_f32_e32 v205, v73
	v_exp_f32_e32 v206, v74
	v_exp_f32_e32 v207, v75
	v_exp_f32_e32 v208, v76
	v_exp_f32_e32 v209, v77
	v_mfma_f32_32x32x16_bf16 v[80:95], v[84:87], v[122:125], 0
	v_exp_f32_e32 v210, v78
	v_exp_f32_e32 v79, v79
	s_waitcnt lgkmcnt(0)
	v_mfma_f32_32x32x16_bf16 v[96:111], v[196:199], v[126:129], v[96:111]
	v_mfma_f32_32x32x16_bf16 v[80:95], v[200:203], v[126:129], v[80:95]
	ds_read_b128 v[196:199], v136 offset:33792
	ds_read_b128 v[200:203], v136 offset:41984
	s_waitcnt lgkmcnt(0)
	v_mfma_f32_32x32x16_bf16 v[96:111], v[196:199], v[118:121], v[96:111]
	v_mfma_f32_32x32x16_bf16 v[80:95], v[200:203], v[118:121], v[80:95]
	ds_read_b128 v[196:199], v137 offset:33792
	ds_read_b128 v[200:203], v137 offset:41984
	v_exp_f32_e32 v180, v64
	v_add_f32_e32 v64, v161, v159
	v_add_f32_e32 v195, v157, v160
	v_add_f32_e32 v64, v155, v64
	v_add_f32_e32 v195, v158, v195
	v_add_f32_e32 v64, v154, v64
	v_add_f32_e32 v195, v156, v195
	v_add_f32_e32 v64, v151, v64
	v_add_f32_e32 v195, v153, v195
	v_add_f32_e32 v64, v149, v64
	v_add_f32_e32 v195, v152, v195
	v_add_f32_e32 v64, v147, v64
	s_waitcnt lgkmcnt(0)
	v_mfma_f32_32x32x16_bf16 v[96:111], v[196:199], v[114:117], v[96:111]
	v_exp_f32_e32 v197, v65
	v_add_f32_e32 v195, v150, v195
	v_exp_f32_e32 v198, v66
	v_add_f32_e32 v64, v146, v64
	v_exp_f32_e32 v199, v67
	v_add_f32_e32 v195, v148, v195
	v_add_f32_e32 v64, v180, v64
	v_mfma_f32_32x32x16_bf16 v[80:95], v[200:203], v[114:117], v[80:95]
	v_exp_f32_e32 v200, v68
	v_exp_f32_e32 v201, v69
	v_add_f32_e32 v195, v197, v195
	v_exp_f32_e32 v202, v70
	v_add_f32_e32 v64, v198, v64
	v_exp_f32_e32 v203, v71
	v_add_f32_e32 v195, v199, v195
	v_add_f32_e32 v64, v200, v64
	v_add_f32_e32 v195, v201, v195
	v_add_f32_e32 v64, v202, v64
	v_add_f32_e32 v195, v203, v195
	v_add_f32_e32 v64, v204, v64
	v_add_f32_e32 v195, v205, v195
	v_add_f32_e32 v64, v206, v64
	v_add_f32_e32 v195, v207, v195
	v_add_f32_e32 v64, v208, v64
	v_add_f32_e32 v195, v209, v195
	v_add_f32_e32 v64, v210, v64
	v_add_f32_e32 v195, v79, v195
	v_add_f32_e32 v195, v195, v64
	v_cvt_pk_bf16_f32 v64, v159, v161
	v_cvt_pk_bf16_f32 v65, v157, v160
	v_cvt_pk_bf16_f32 v66, v155, v158
	v_cvt_pk_bf16_f32 v67, v154, v156
	v_cvt_pk_bf16_f32 v68, v151, v153
	v_cvt_pk_bf16_f32 v69, v149, v152
	v_cvt_pk_bf16_f32 v70, v147, v150
	v_cvt_pk_bf16_f32 v71, v146, v148
	v_cvt_pk_bf16_f32 v72, v180, v197
	v_cvt_pk_bf16_f32 v73, v198, v199
	v_cvt_pk_bf16_f32 v74, v200, v201
	v_cvt_pk_bf16_f32 v75, v202, v203
	v_cvt_pk_bf16_f32 v76, v204, v205
	v_cvt_pk_bf16_f32 v77, v206, v207
	v_cvt_pk_bf16_f32 v78, v208, v209
	v_cvt_pk_bf16_f32 v79, v210, v79
	s_add_i32 m0, s84, 0x8400
	s_add_u32 s66, s78, s65
	s_addc_u32 s67, s79, 0
	global_load_lds_dwordx4 v185, s[66:67]
	s_add_i32 m0, s84, 0xa400
	s_add_i32 s64, s65, 0x60000
	global_load_lds_dwordx4 v184, s[66:67]
	s_add_i32 m0, s84, 0xc400
	s_add_u32 s70, s80, s64
	s_addc_u32 s71, s81, 0
	global_load_lds_dwordx4 v183, s[70:71]
	s_add_i32 m0, s84, 0xe400
	s_mov_b32 s65, s64
	global_load_lds_dwordx4 v182, s[70:71]
	ds_read_b64_tr_b16 v[198:199], v192 offset:1024
	ds_read_b64_tr_b16 v[200:201], v192 offset:3072
	ds_read_b64_tr_b16 v[202:203], v192 offset:5120
	ds_read_b64_tr_b16 v[204:205], v192 offset:7168
	ds_read_b64_tr_b16 v[206:207], v192 offset:9216
	ds_read_b64_tr_b16 v[208:209], v192 offset:11264
	ds_read_b64_tr_b16 v[222:223], v192 offset:13312
	ds_read_b64_tr_b16 v[224:225], v192 offset:15360
	s_waitcnt lgkmcnt(0)
	v_mfma_f32_32x32x16_bf16 v[0:15], v[64:67], v[198:201], v[0:15]
	ds_read_b64_tr_b16 v[198:199], v192 offset:1536
	ds_read_b64_tr_b16 v[200:201], v192 offset:3584
	v_mfma_f32_32x32x16_bf16 v[0:15], v[68:71], v[202:205], v[0:15]
	ds_read_b64_tr_b16 v[202:203], v192 offset:5632
	ds_read_b64_tr_b16 v[204:205], v192 offset:7680
	v_mfma_f32_32x32x16_bf16 v[0:15], v[72:75], v[206:209], v[0:15]
	ds_read_b64_tr_b16 v[206:207], v192 offset:9728
	ds_read_b64_tr_b16 v[208:209], v192 offset:11776
	v_mfma_f32_32x32x16_bf16 v[0:15], v[76:79], v[222:225], v[0:15]
	ds_read_b64_tr_b16 v[222:223], v192 offset:13824
	ds_read_b64_tr_b16 v[224:225], v192 offset:15872
	s_waitcnt lgkmcnt(0)
	v_mfma_f32_32x32x16_bf16 v[48:63], v[64:67], v[198:201], v[48:63]
	ds_read_b64_tr_b16 v[198:199], v192 offset:2048
	ds_read_b64_tr_b16 v[200:201], v192 offset:4096
	v_mfma_f32_32x32x16_bf16 v[48:63], v[68:71], v[202:205], v[48:63]
	ds_read_b64_tr_b16 v[202:203], v192 offset:6144
	ds_read_b64_tr_b16 v[204:205], v192 offset:8192
	v_mfma_f32_32x32x16_bf16 v[48:63], v[72:75], v[206:209], v[48:63]
	ds_read_b64_tr_b16 v[206:207], v192 offset:10240
	ds_read_b64_tr_b16 v[208:209], v192 offset:12288
	v_mfma_f32_32x32x16_bf16 v[48:63], v[76:79], v[222:225], v[48:63]
	ds_read_b64_tr_b16 v[222:223], v192 offset:14336
	ds_read_b64_tr_b16 v[224:225], v192 offset:16384
	s_waitcnt lgkmcnt(0)
	v_mfma_f32_32x32x16_bf16 v[32:47], v[64:67], v[198:201], v[32:47]
	ds_read_b64_tr_b16 v[198:199], v192 offset:2560
	ds_read_b64_tr_b16 v[200:201], v192 offset:4608
	v_mfma_f32_32x32x16_bf16 v[32:47], v[68:71], v[202:205], v[32:47]
	ds_read_b64_tr_b16 v[202:203], v192 offset:6656
	ds_read_b64_tr_b16 v[204:205], v192 offset:8704
	v_mfma_f32_32x32x16_bf16 v[32:47], v[72:75], v[206:209], v[32:47]
	ds_read_b64_tr_b16 v[206:207], v192 offset:10752
	ds_read_b64_tr_b16 v[208:209], v192 offset:12800
	v_mfma_f32_32x32x16_bf16 v[32:47], v[76:79], v[222:225], v[32:47]
	ds_read_b64_tr_b16 v[222:223], v192 offset:14848
	ds_read_b64_tr_b16 v[224:225], v192 offset:16896
	s_waitcnt lgkmcnt(0)
	v_mfma_f32_32x32x16_bf16 v[16:31], v[64:67], v[198:201], v[16:31]
	v_max_f32_e32 v64, v96, v97
	v_max3_f32 v65, v80, v81, v82
	v_max3_f32 v64, v64, v98, v99
	v_max3_f32 v65, v65, v83, v84
	v_max3_f32 v64, v64, v100, v101
	v_mfma_f32_32x32x16_bf16 v[16:31], v[68:71], v[202:205], v[16:31]
	v_max3_f32 v65, v65, v85, v86
	v_max3_f32 v64, v64, v102, v103
	v_max3_f32 v65, v65, v87, v88
	v_max3_f32 v64, v64, v104, v105
	v_max3_f32 v65, v65, v89, v90
	v_max3_f32 v64, v64, v106, v107
	v_max3_f32 v65, v65, v91, v92
	v_mfma_f32_32x32x16_bf16 v[16:31], v[72:75], v[206:209], v[16:31]
	v_max3_f32 v64, v64, v108, v109
	v_max3_f32 v65, v65, v93, v94
	v_max3_f32 v64, v64, v110, v111
	v_max3_f32 v64, v64, v65, v95
	v_mov_b32_e32 v198, 1.0
	v_mfma_f32_32x32x16_bf16 v[16:31], v[76:79], v[222:225], v[16:31]
	v_cmp_ge_f32_e64 s[0:1], s56, v64
	s_cmp_eq_u64 s[0:1], exec
	s_cbranch_scc1 .LBB0_792
	s_branch .LBB0_801

.LBB0_792:
	v_exp_f32_e32 v197, v96
	v_exp_f32_e32 v208, v97
	v_exp_f32_e32 v209, v98
	v_exp_f32_e32 v210, v99
	v_exp_f32_e32 v211, v100
	v_exp_f32_e32 v220, v101
	v_exp_f32_e32 v221, v102
	v_exp_f32_e32 v222, v103
	v_exp_f32_e32 v223, v104
	v_exp_f32_e32 v224, v105
	v_exp_f32_e32 v225, v106
	v_exp_f32_e32 v226, v107
	v_exp_f32_e32 v227, v108
	v_exp_f32_e32 v228, v109
	v_exp_f32_e32 v229, v110
	v_exp_f32_e32 v230, v111
	s_waitcnt vmcnt(4) lgkmcnt(0)
	s_barrier
	ds_read_b128 v[64:67], v134 offset:50176
	ds_read_b128 v[68:71], v134 offset:58368
	ds_read_b128 v[200:203], v135 offset:50176
	ds_read_b128 v[204:207], v135 offset:58368
	v_exp_f32_e32 v231, v87
	s_waitcnt lgkmcnt(2)
	v_mfma_f32_32x32x16_bf16 v[96:111], v[64:67], v[122:125], 0
	v_exp_f32_e32 v232, v88
	v_exp_f32_e32 v233, v89
	v_exp_f32_e32 v234, v90
	v_exp_f32_e32 v235, v91
	v_exp_f32_e32 v236, v92
	v_exp_f32_e32 v237, v93
	v_exp_f32_e32 v238, v94
	v_mfma_f32_32x32x16_bf16 v[64:79], v[68:71], v[122:125], 0
	v_exp_f32_e32 v95, v95
	s_waitcnt lgkmcnt(0)
	v_mfma_f32_32x32x16_bf16 v[96:111], v[200:203], v[126:129], v[96:111]
	v_mfma_f32_32x32x16_bf16 v[64:79], v[204:207], v[126:129], v[64:79]
	ds_read_b128 v[200:203], v136 offset:50176
	ds_read_b128 v[204:207], v136 offset:58368
	s_waitcnt lgkmcnt(0)
	v_mfma_f32_32x32x16_bf16 v[96:111], v[200:203], v[118:121], v[96:111]
	v_mfma_f32_32x32x16_bf16 v[64:79], v[204:207], v[118:121], v[64:79]
	ds_read_b128 v[200:203], v137 offset:50176
	ds_read_b128 v[204:207], v137 offset:58368
	s_waitcnt lgkmcnt(0)
	v_mfma_f32_32x32x16_bf16 v[96:111], v[200:203], v[114:117], v[96:111]
	v_exp_f32_e32 v201, v80
	v_add_f32_e32 v80, v208, v197
	v_add_f32_e32 v199, v209, v210
	v_add_f32_e32 v80, v211, v80
	v_add_f32_e32 v199, v220, v199
	v_add_f32_e32 v80, v221, v80
	v_add_f32_e32 v199, v222, v199
	v_add_f32_e32 v80, v223, v80
	v_add_f32_e32 v199, v224, v199
	v_add_f32_e32 v80, v225, v80
	v_add_f32_e32 v199, v226, v199
	v_add_f32_e32 v80, v227, v80
	v_exp_f32_e32 v202, v81
	v_add_f32_e32 v199, v228, v199
	v_exp_f32_e32 v203, v82
	v_add_f32_e32 v80, v229, v80
	v_mfma_f32_32x32x16_bf16 v[64:79], v[204:207], v[114:117], v[64:79]
	v_exp_f32_e32 v204, v83
	v_add_f32_e32 v199, v230, v199
	v_exp_f32_e32 v205, v84
	v_add_f32_e32 v80, v201, v80
	v_exp_f32_e32 v206, v85
	v_add_f32_e32 v199, v202, v199
	v_exp_f32_e32 v207, v86
	v_add_f32_e32 v80, v203, v80
	v_add_f32_e32 v199, v204, v199
	v_add_f32_e32 v80, v205, v80
	v_add_f32_e32 v199, v206, v199
	v_add_f32_e32 v80, v207, v80
	v_add_f32_e32 v199, v231, v199
	v_add_f32_e32 v80, v232, v80
	v_add_f32_e32 v199, v233, v199
	v_add_f32_e32 v80, v234, v80
	v_add_f32_e32 v199, v235, v199
	v_add_f32_e32 v80, v236, v80
	v_add_f32_e32 v199, v237, v199
	v_add_f32_e32 v80, v238, v80
	v_add_f32_e32 v199, v95, v199
	v_add_f32_e32 v199, v199, v80
	v_cvt_pk_bf16_f32 v80, v197, v208
	v_cvt_pk_bf16_f32 v81, v209, v210
	v_cvt_pk_bf16_f32 v82, v211, v220
	v_cvt_pk_bf16_f32 v83, v221, v222
	v_cvt_pk_bf16_f32 v84, v223, v224
	v_cvt_pk_bf16_f32 v85, v225, v226
	v_cvt_pk_bf16_f32 v86, v227, v228
	v_cvt_pk_bf16_f32 v87, v229, v230
	v_cvt_pk_bf16_f32 v88, v201, v202
	v_cvt_pk_bf16_f32 v89, v203, v204
	v_cvt_pk_bf16_f32 v90, v205, v206
	v_cvt_pk_bf16_f32 v91, v207, v231
	v_cvt_pk_bf16_f32 v92, v232, v233
	v_cvt_pk_bf16_f32 v93, v234, v235
	v_cvt_pk_bf16_f32 v94, v236, v237
	v_cvt_pk_bf16_f32 v95, v238, v95
	s_add_i32 m0, s84, 0x400
	s_add_u32 s66, s78, s65
	s_addc_u32 s67, s79, 0
	global_load_lds_dwordx4 v185, s[66:67]
	s_add_i32 m0, s84, 0x2400
	s_add_i32 s64, s65, 0x60000
	global_load_lds_dwordx4 v184, s[66:67]
	s_cmp_eq_u32 s55, 29
	s_cselect_b32 s64, s89, s64
	s_add_i32 m0, s84, 0x10400
	s_add_u32 s70, s80, s64
	s_addc_u32 s71, s81, 0
	global_load_lds_dwordx4 v183, s[70:71]
	s_add_i32 m0, s84, 0x12400
	s_mov_b32 s65, s64
	global_load_lds_dwordx4 v182, s[70:71]
.LBB0_794:
	ds_read_b64_tr_b16 v[202:203], v192 offset:17408
	ds_read_b64_tr_b16 v[204:205], v192 offset:19456
	ds_read_b64_tr_b16 v[206:207], v192 offset:21504
	ds_read_b64_tr_b16 v[208:209], v192 offset:23552
	ds_read_b64_tr_b16 v[222:223], v192 offset:25600
	ds_read_b64_tr_b16 v[224:225], v192 offset:27648
	ds_read_b64_tr_b16 v[226:227], v192 offset:29696
	ds_read_b64_tr_b16 v[228:229], v192 offset:31744
	s_waitcnt lgkmcnt(0)
	v_mfma_f32_32x32x16_bf16 v[0:15], v[80:83], v[202:205], v[0:15]
	ds_read_b64_tr_b16 v[202:203], v192 offset:17920
	ds_read_b64_tr_b16 v[204:205], v192 offset:19968
	v_mfma_f32_32x32x16_bf16 v[0:15], v[84:87], v[206:209], v[0:15]
	ds_read_b64_tr_b16 v[206:207], v192 offset:22016
	ds_read_b64_tr_b16 v[208:209], v192 offset:24064
	v_mfma_f32_32x32x16_bf16 v[0:15], v[88:91], v[222:225], v[0:15]
	ds_read_b64_tr_b16 v[222:223], v192 offset:26112
	ds_read_b64_tr_b16 v[224:225], v192 offset:28160
	v_mfma_f32_32x32x16_bf16 v[0:15], v[92:95], v[226:229], v[0:15]
	ds_read_b64_tr_b16 v[226:227], v192 offset:30208
	ds_read_b64_tr_b16 v[228:229], v192 offset:32256
	s_waitcnt lgkmcnt(0)
	v_mfma_f32_32x32x16_bf16 v[48:63], v[80:83], v[202:205], v[48:63]
	ds_read_b64_tr_b16 v[202:203], v192 offset:18432
	ds_read_b64_tr_b16 v[204:205], v192 offset:20480
	v_mfma_f32_32x32x16_bf16 v[48:63], v[84:87], v[206:209], v[48:63]
	ds_read_b64_tr_b16 v[206:207], v192 offset:22528
	ds_read_b64_tr_b16 v[208:209], v192 offset:24576
	v_mfma_f32_32x32x16_bf16 v[48:63], v[88:91], v[222:225], v[48:63]
	ds_read_b64_tr_b16 v[222:223], v192 offset:26624
	ds_read_b64_tr_b16 v[224:225], v192 offset:28672
	v_mfma_f32_32x32x16_bf16 v[48:63], v[92:95], v[226:229], v[48:63]
	ds_read_b64_tr_b16 v[226:227], v192 offset:30720
	ds_read_b64_tr_b16 v[228:229], v192 offset:32768
	s_waitcnt lgkmcnt(0)
	v_mfma_f32_32x32x16_bf16 v[32:47], v[80:83], v[202:205], v[32:47]
	ds_read_b64_tr_b16 v[202:203], v192 offset:18944
	ds_read_b64_tr_b16 v[204:205], v192 offset:20992
	v_mfma_f32_32x32x16_bf16 v[32:47], v[84:87], v[206:209], v[32:47]
	ds_read_b64_tr_b16 v[206:207], v192 offset:23040
	ds_read_b64_tr_b16 v[208:209], v192 offset:25088
	v_mfma_f32_32x32x16_bf16 v[32:47], v[88:91], v[222:225], v[32:47]
	ds_read_b64_tr_b16 v[222:223], v192 offset:27136
	ds_read_b64_tr_b16 v[224:225], v192 offset:29184
	v_mfma_f32_32x32x16_bf16 v[32:47], v[92:95], v[226:229], v[32:47]
	ds_read_b64_tr_b16 v[226:227], v192 offset:31232
	ds_read_b64_tr_b16 v[228:229], v192 offset:33280
	s_waitcnt lgkmcnt(0)
	v_mfma_f32_32x32x16_bf16 v[16:31], v[80:83], v[202:205], v[16:31]
	v_max_f32_e32 v80, v96, v97
	v_max3_f32 v81, v64, v65, v66
	v_max3_f32 v80, v80, v98, v99
	v_max3_f32 v81, v81, v67, v68
	v_max3_f32 v80, v80, v100, v101
	v_mfma_f32_32x32x16_bf16 v[16:31], v[84:87], v[206:209], v[16:31]
	v_max3_f32 v81, v81, v69, v70
	v_max3_f32 v80, v80, v102, v103
	v_max3_f32 v81, v81, v71, v72
	v_max3_f32 v80, v80, v104, v105
	v_max3_f32 v81, v81, v73, v74
	v_max3_f32 v80, v80, v106, v107
	v_max3_f32 v81, v81, v75, v76
	v_mfma_f32_32x32x16_bf16 v[16:31], v[88:91], v[222:225], v[16:31]
	v_max3_f32 v80, v80, v108, v109
	v_max3_f32 v81, v81, v77, v78
	v_max3_f32 v80, v80, v110, v111
	v_max3_f32 v80, v80, v81, v79
	v_mov_b32_e32 v197, 1.0
	v_mfma_f32_32x32x16_bf16 v[16:31], v[92:95], v[226:229], v[16:31]
	v_cmp_ge_f32_e64 s[0:1], s56, v80
	s_cmp_eq_u64 s[0:1], exec
	s_cbranch_scc1 .LBB0_799
	s_branch .LBB0_802

.LBB0_799:
	v_exp_f32_e32 v159, v96
	v_exp_f32_e32 v161, v97
	v_exp_f32_e32 v157, v98
	v_exp_f32_e32 v160, v99
	v_exp_f32_e32 v155, v100
	v_exp_f32_e32 v158, v101
	v_exp_f32_e32 v154, v102
	v_exp_f32_e32 v156, v103
	v_exp_f32_e32 v151, v104
	v_exp_f32_e32 v153, v105
	v_exp_f32_e32 v149, v106
	v_exp_f32_e32 v152, v107
	v_exp_f32_e32 v147, v108
	v_exp_f32_e32 v150, v109
	v_exp_f32_e32 v146, v110
	v_exp_f32_e32 v148, v111
	v_fma_f32 v80, v193, v179, v195
	v_fma_f32 v179, v80, v198, v199
	s_cmp_gt_u32 s55, 32
	s_waitcnt vmcnt(4) lgkmcnt(0)
	s_barrier
	s_cbranch_scc1 .LBB0_803
	s_add_i32 s55, s55, 2
	v_mov_b32_e32 v193, v197
	ds_read_b128 v[80:83], v130 offset:50176
	ds_read_b128 v[84:87], v130 offset:58368
	ds_read_b128 v[196:199], v131 offset:50176
	ds_read_b128 v[200:203], v131 offset:58368
	s_waitcnt lgkmcnt(2)
	v_mfma_f32_32x32x16_bf16 v[96:111], v[80:83], v[122:125], 0
	v_exp_f32_e32 v204, v72
	v_exp_f32_e32 v205, v73
	v_exp_f32_e32 v206, v74
	v_exp_f32_e32 v207, v75
	v_exp_f32_e32 v208, v76
	v_exp_f32_e32 v209, v77
	v_mfma_f32_32x32x16_bf16 v[80:95], v[84:87], v[122:125], 0
	v_exp_f32_e32 v210, v78
	v_exp_f32_e32 v79, v79
	s_waitcnt lgkmcnt(0)
	v_mfma_f32_32x32x16_bf16 v[96:111], v[196:199], v[126:129], v[96:111]
	v_mfma_f32_32x32x16_bf16 v[80:95], v[200:203], v[126:129], v[80:95]
	ds_read_b128 v[196:199], v132 offset:50176
	ds_read_b128 v[200:203], v132 offset:58368
	s_waitcnt lgkmcnt(0)
	v_mfma_f32_32x32x16_bf16 v[96:111], v[196:199], v[118:121], v[96:111]
	v_mfma_f32_32x32x16_bf16 v[80:95], v[200:203], v[118:121], v[80:95]
	ds_read_b128 v[196:199], v133 offset:50176
	ds_read_b128 v[200:203], v133 offset:58368
	v_exp_f32_e32 v180, v64
	v_add_f32_e32 v64, v161, v159
	v_add_f32_e32 v195, v157, v160
	v_add_f32_e32 v64, v155, v64
	v_add_f32_e32 v195, v158, v195
	v_add_f32_e32 v64, v154, v64
	v_add_f32_e32 v195, v156, v195
	v_add_f32_e32 v64, v151, v64
	v_add_f32_e32 v195, v153, v195
	v_add_f32_e32 v64, v149, v64
	v_add_f32_e32 v195, v152, v195
	v_add_f32_e32 v64, v147, v64
	s_waitcnt lgkmcnt(0)
	v_mfma_f32_32x32x16_bf16 v[96:111], v[196:199], v[114:117], v[96:111]
	v_exp_f32_e32 v197, v65
	v_add_f32_e32 v195, v150, v195
	v_exp_f32_e32 v198, v66
	v_add_f32_e32 v64, v146, v64
	v_exp_f32_e32 v199, v67
	v_add_f32_e32 v195, v148, v195
	v_add_f32_e32 v64, v180, v64
	v_mfma_f32_32x32x16_bf16 v[80:95], v[200:203], v[114:117], v[80:95]
	v_exp_f32_e32 v200, v68
	v_exp_f32_e32 v201, v69
	v_add_f32_e32 v195, v197, v195
	v_exp_f32_e32 v202, v70
	v_add_f32_e32 v64, v198, v64
	v_exp_f32_e32 v203, v71
	v_add_f32_e32 v195, v199, v195
	v_add_f32_e32 v64, v200, v64
	v_add_f32_e32 v195, v201, v195
	v_add_f32_e32 v64, v202, v64
	v_add_f32_e32 v195, v203, v195
	v_add_f32_e32 v64, v204, v64
	v_add_f32_e32 v195, v205, v195
	v_add_f32_e32 v64, v206, v64
	v_add_f32_e32 v195, v207, v195
	v_add_f32_e32 v64, v208, v64
	v_add_f32_e32 v195, v209, v195
	v_add_f32_e32 v64, v210, v64
	v_add_f32_e32 v195, v79, v195
	v_add_f32_e32 v195, v195, v64
	v_cvt_pk_bf16_f32 v64, v159, v161
	v_cvt_pk_bf16_f32 v65, v157, v160
	v_cvt_pk_bf16_f32 v66, v155, v158
	v_cvt_pk_bf16_f32 v67, v154, v156
	v_cvt_pk_bf16_f32 v68, v151, v153
	v_cvt_pk_bf16_f32 v69, v149, v152
	v_cvt_pk_bf16_f32 v70, v147, v150
	v_cvt_pk_bf16_f32 v71, v146, v148
	v_cvt_pk_bf16_f32 v72, v180, v197
	v_cvt_pk_bf16_f32 v73, v198, v199
	v_cvt_pk_bf16_f32 v74, v200, v201
	v_cvt_pk_bf16_f32 v75, v202, v203
	v_cvt_pk_bf16_f32 v76, v204, v205
	v_cvt_pk_bf16_f32 v77, v206, v207
	v_cvt_pk_bf16_f32 v78, v208, v209
	v_cvt_pk_bf16_f32 v79, v210, v79
	s_add_i32 m0, s84, 0x4400
	s_add_u32 s66, s78, s65
	s_addc_u32 s67, s79, 0
	global_load_lds_dwordx4 v185, s[66:67]
	s_add_i32 m0, s84, 0x6400
	s_add_i32 s64, s65, 0x60000
	global_load_lds_dwordx4 v184, s[66:67]
	s_add_i32 m0, s84, 0x14400
	s_add_u32 s70, s80, s64
	s_addc_u32 s71, s81, 0
	global_load_lds_dwordx4 v183, s[70:71]
	s_add_i32 m0, s84, 0x16400
	s_mov_b32 s65, s64
	global_load_lds_dwordx4 v182, s[70:71]
	ds_read_b64_tr_b16 v[198:199], v192 offset:33792
	ds_read_b64_tr_b16 v[200:201], v192 offset:35840
	ds_read_b64_tr_b16 v[202:203], v192 offset:37888
	ds_read_b64_tr_b16 v[204:205], v192 offset:39936
	ds_read_b64_tr_b16 v[206:207], v192 offset:41984
	ds_read_b64_tr_b16 v[208:209], v192 offset:44032
	ds_read_b64_tr_b16 v[222:223], v192 offset:46080
	ds_read_b64_tr_b16 v[224:225], v192 offset:48128
	s_waitcnt lgkmcnt(0)
	v_mfma_f32_32x32x16_bf16 v[0:15], v[64:67], v[198:201], v[0:15]
	ds_read_b64_tr_b16 v[198:199], v192 offset:34304
	ds_read_b64_tr_b16 v[200:201], v192 offset:36352
	v_mfma_f32_32x32x16_bf16 v[0:15], v[68:71], v[202:205], v[0:15]
	ds_read_b64_tr_b16 v[202:203], v192 offset:38400
	ds_read_b64_tr_b16 v[204:205], v192 offset:40448
	v_mfma_f32_32x32x16_bf16 v[0:15], v[72:75], v[206:209], v[0:15]
	ds_read_b64_tr_b16 v[206:207], v192 offset:42496
	ds_read_b64_tr_b16 v[208:209], v192 offset:44544
	v_mfma_f32_32x32x16_bf16 v[0:15], v[76:79], v[222:225], v[0:15]
	ds_read_b64_tr_b16 v[222:223], v192 offset:46592
	ds_read_b64_tr_b16 v[224:225], v192 offset:48640
	s_waitcnt lgkmcnt(0)
	v_mfma_f32_32x32x16_bf16 v[48:63], v[64:67], v[198:201], v[48:63]
	ds_read_b64_tr_b16 v[198:199], v192 offset:34816
	ds_read_b64_tr_b16 v[200:201], v192 offset:36864
	v_mfma_f32_32x32x16_bf16 v[48:63], v[68:71], v[202:205], v[48:63]
	ds_read_b64_tr_b16 v[202:203], v192 offset:38912
	ds_read_b64_tr_b16 v[204:205], v192 offset:40960
	v_mfma_f32_32x32x16_bf16 v[48:63], v[72:75], v[206:209], v[48:63]
	ds_read_b64_tr_b16 v[206:207], v192 offset:43008
	ds_read_b64_tr_b16 v[208:209], v192 offset:45056
	v_mfma_f32_32x32x16_bf16 v[48:63], v[76:79], v[222:225], v[48:63]
	ds_read_b64_tr_b16 v[222:223], v192 offset:47104
	ds_read_b64_tr_b16 v[224:225], v192 offset:49152
	s_waitcnt lgkmcnt(0)
	v_mfma_f32_32x32x16_bf16 v[32:47], v[64:67], v[198:201], v[32:47]
	ds_read_b64_tr_b16 v[198:199], v192 offset:35328
	ds_read_b64_tr_b16 v[200:201], v192 offset:37376
	v_mfma_f32_32x32x16_bf16 v[32:47], v[68:71], v[202:205], v[32:47]
	ds_read_b64_tr_b16 v[202:203], v192 offset:39424
	ds_read_b64_tr_b16 v[204:205], v192 offset:41472
	v_mfma_f32_32x32x16_bf16 v[32:47], v[72:75], v[206:209], v[32:47]
	ds_read_b64_tr_b16 v[206:207], v192 offset:43520
	ds_read_b64_tr_b16 v[208:209], v192 offset:45568
	v_mfma_f32_32x32x16_bf16 v[32:47], v[76:79], v[222:225], v[32:47]
	ds_read_b64_tr_b16 v[222:223], v192 offset:47616
	ds_read_b64_tr_b16 v[224:225], v192 offset:49664
	s_waitcnt lgkmcnt(0)
	v_mfma_f32_32x32x16_bf16 v[16:31], v[64:67], v[198:201], v[16:31]
	v_max_f32_e32 v64, v96, v97
	v_max3_f32 v65, v80, v81, v82
	v_max3_f32 v64, v64, v98, v99
	v_max3_f32 v65, v65, v83, v84
	v_max3_f32 v64, v64, v100, v101
	v_mfma_f32_32x32x16_bf16 v[16:31], v[68:71], v[202:205], v[16:31]
	v_max3_f32 v65, v65, v85, v86
	v_max3_f32 v64, v64, v102, v103
	v_max3_f32 v65, v65, v87, v88
	v_max3_f32 v64, v64, v104, v105
	v_max3_f32 v65, v65, v89, v90
	v_max3_f32 v64, v64, v106, v107
	v_max3_f32 v65, v65, v91, v92
	v_mfma_f32_32x32x16_bf16 v[16:31], v[72:75], v[206:209], v[16:31]
	v_max3_f32 v64, v64, v108, v109
	v_max3_f32 v65, v65, v93, v94
	v_max3_f32 v64, v64, v110, v111
	v_max3_f32 v64, v64, v65, v95
	v_mov_b32_e32 v198, 1.0
	v_mfma_f32_32x32x16_bf16 v[16:31], v[76:79], v[222:225], v[16:31]
	v_cmp_ge_f32_e64 s[0:1], s56, v64
	s_cmp_eq_u64 s[0:1], exec
	s_cbranch_scc1 .Lc1_792
	s_branch .Lc1_801

.Lc1_792:
	v_exp_f32_e32 v197, v96
	v_exp_f32_e32 v208, v97
	v_exp_f32_e32 v209, v98
	v_exp_f32_e32 v210, v99
	v_exp_f32_e32 v211, v100
	v_exp_f32_e32 v220, v101
	v_exp_f32_e32 v221, v102
	v_exp_f32_e32 v222, v103
	v_exp_f32_e32 v223, v104
	v_exp_f32_e32 v224, v105
	v_exp_f32_e32 v225, v106
	v_exp_f32_e32 v226, v107
	v_exp_f32_e32 v227, v108
	v_exp_f32_e32 v228, v109
	v_exp_f32_e32 v229, v110
	v_exp_f32_e32 v230, v111
	s_waitcnt vmcnt(4) lgkmcnt(0)
	s_barrier
	ds_read_b128 v[64:67], v134 offset:33792
	ds_read_b128 v[68:71], v134 offset:41984
	ds_read_b128 v[200:203], v135 offset:33792
	ds_read_b128 v[204:207], v135 offset:41984
	v_exp_f32_e32 v231, v87
	s_waitcnt lgkmcnt(2)
	v_mfma_f32_32x32x16_bf16 v[96:111], v[64:67], v[122:125], 0
	v_exp_f32_e32 v232, v88
	v_exp_f32_e32 v233, v89
	v_exp_f32_e32 v234, v90
	v_exp_f32_e32 v235, v91
	v_exp_f32_e32 v236, v92
	v_exp_f32_e32 v237, v93
	v_exp_f32_e32 v238, v94
	v_mfma_f32_32x32x16_bf16 v[64:79], v[68:71], v[122:125], 0
	v_exp_f32_e32 v95, v95
	s_waitcnt lgkmcnt(0)
	v_mfma_f32_32x32x16_bf16 v[96:111], v[200:203], v[126:129], v[96:111]
	v_mfma_f32_32x32x16_bf16 v[64:79], v[204:207], v[126:129], v[64:79]
	ds_read_b128 v[200:203], v136 offset:33792
	ds_read_b128 v[204:207], v136 offset:41984
	s_waitcnt lgkmcnt(0)
	v_mfma_f32_32x32x16_bf16 v[96:111], v[200:203], v[118:121], v[96:111]
	v_mfma_f32_32x32x16_bf16 v[64:79], v[204:207], v[118:121], v[64:79]
	ds_read_b128 v[200:203], v137 offset:33792
	ds_read_b128 v[204:207], v137 offset:41984
	s_waitcnt lgkmcnt(0)
	v_mfma_f32_32x32x16_bf16 v[96:111], v[200:203], v[114:117], v[96:111]
	v_exp_f32_e32 v201, v80
	v_add_f32_e32 v80, v208, v197
	v_add_f32_e32 v199, v209, v210
	v_add_f32_e32 v80, v211, v80
	v_add_f32_e32 v199, v220, v199
	v_add_f32_e32 v80, v221, v80
	v_add_f32_e32 v199, v222, v199
	v_add_f32_e32 v80, v223, v80
	v_add_f32_e32 v199, v224, v199
	v_add_f32_e32 v80, v225, v80
	v_add_f32_e32 v199, v226, v199
	v_add_f32_e32 v80, v227, v80
	v_exp_f32_e32 v202, v81
	v_add_f32_e32 v199, v228, v199
	v_exp_f32_e32 v203, v82
	v_add_f32_e32 v80, v229, v80
	v_mfma_f32_32x32x16_bf16 v[64:79], v[204:207], v[114:117], v[64:79]
	v_exp_f32_e32 v204, v83
	v_add_f32_e32 v199, v230, v199
	v_exp_f32_e32 v205, v84
	v_add_f32_e32 v80, v201, v80
	v_exp_f32_e32 v206, v85
	v_add_f32_e32 v199, v202, v199
	v_exp_f32_e32 v207, v86
	v_add_f32_e32 v80, v203, v80
	v_add_f32_e32 v199, v204, v199
	v_add_f32_e32 v80, v205, v80
	v_add_f32_e32 v199, v206, v199
	v_add_f32_e32 v80, v207, v80
	v_add_f32_e32 v199, v231, v199
	v_add_f32_e32 v80, v232, v80
	v_add_f32_e32 v199, v233, v199
	v_add_f32_e32 v80, v234, v80
	v_add_f32_e32 v199, v235, v199
	v_add_f32_e32 v80, v236, v80
	v_add_f32_e32 v199, v237, v199
	v_add_f32_e32 v80, v238, v80
	v_add_f32_e32 v199, v95, v199
	v_add_f32_e32 v199, v199, v80
	v_cvt_pk_bf16_f32 v80, v197, v208
	v_cvt_pk_bf16_f32 v81, v209, v210
	v_cvt_pk_bf16_f32 v82, v211, v220
	v_cvt_pk_bf16_f32 v83, v221, v222
	v_cvt_pk_bf16_f32 v84, v223, v224
	v_cvt_pk_bf16_f32 v85, v225, v226
	v_cvt_pk_bf16_f32 v86, v227, v228
	v_cvt_pk_bf16_f32 v87, v229, v230
	v_cvt_pk_bf16_f32 v88, v201, v202
	v_cvt_pk_bf16_f32 v89, v203, v204
	v_cvt_pk_bf16_f32 v90, v205, v206
	v_cvt_pk_bf16_f32 v91, v207, v231
	v_cvt_pk_bf16_f32 v92, v232, v233
	v_cvt_pk_bf16_f32 v93, v234, v235
	v_cvt_pk_bf16_f32 v94, v236, v237
	v_cvt_pk_bf16_f32 v95, v238, v95
	s_add_i32 m0, s84, 0x8400
	s_add_u32 s66, s78, s65
	s_addc_u32 s67, s79, 0
	global_load_lds_dwordx4 v185, s[66:67]
	s_add_i32 m0, s84, 0xa400
	s_add_i32 s64, s65, 0x60000
	global_load_lds_dwordx4 v184, s[66:67]
	s_cmp_eq_u32 s55, 29
	s_cselect_b32 s64, s89, s64
	s_add_i32 m0, s84, 0xc400
	s_add_u32 s70, s80, s64
	s_addc_u32 s71, s81, 0
	global_load_lds_dwordx4 v183, s[70:71]
	s_add_i32 m0, s84, 0xe400
	s_mov_b32 s65, s64
	global_load_lds_dwordx4 v182, s[70:71]
.Lc1_794:
	ds_read_b64_tr_b16 v[202:203], v192 offset:1024
	ds_read_b64_tr_b16 v[204:205], v192 offset:3072
	ds_read_b64_tr_b16 v[206:207], v192 offset:5120
	ds_read_b64_tr_b16 v[208:209], v192 offset:7168
	ds_read_b64_tr_b16 v[222:223], v192 offset:9216
	ds_read_b64_tr_b16 v[224:225], v192 offset:11264
	ds_read_b64_tr_b16 v[226:227], v192 offset:13312
	ds_read_b64_tr_b16 v[228:229], v192 offset:15360
	s_waitcnt lgkmcnt(0)
	v_mfma_f32_32x32x16_bf16 v[0:15], v[80:83], v[202:205], v[0:15]
	ds_read_b64_tr_b16 v[202:203], v192 offset:1536
	ds_read_b64_tr_b16 v[204:205], v192 offset:3584
	v_mfma_f32_32x32x16_bf16 v[0:15], v[84:87], v[206:209], v[0:15]
	ds_read_b64_tr_b16 v[206:207], v192 offset:5632
	ds_read_b64_tr_b16 v[208:209], v192 offset:7680
	v_mfma_f32_32x32x16_bf16 v[0:15], v[88:91], v[222:225], v[0:15]
	ds_read_b64_tr_b16 v[222:223], v192 offset:9728
	ds_read_b64_tr_b16 v[224:225], v192 offset:11776
	v_mfma_f32_32x32x16_bf16 v[0:15], v[92:95], v[226:229], v[0:15]
	ds_read_b64_tr_b16 v[226:227], v192 offset:13824
	ds_read_b64_tr_b16 v[228:229], v192 offset:15872
	s_waitcnt lgkmcnt(0)
	v_mfma_f32_32x32x16_bf16 v[48:63], v[80:83], v[202:205], v[48:63]
	ds_read_b64_tr_b16 v[202:203], v192 offset:2048
	ds_read_b64_tr_b16 v[204:205], v192 offset:4096
	v_mfma_f32_32x32x16_bf16 v[48:63], v[84:87], v[206:209], v[48:63]
	ds_read_b64_tr_b16 v[206:207], v192 offset:6144
	ds_read_b64_tr_b16 v[208:209], v192 offset:8192
	v_mfma_f32_32x32x16_bf16 v[48:63], v[88:91], v[222:225], v[48:63]
	ds_read_b64_tr_b16 v[222:223], v192 offset:10240
	ds_read_b64_tr_b16 v[224:225], v192 offset:12288
	v_mfma_f32_32x32x16_bf16 v[48:63], v[92:95], v[226:229], v[48:63]
	ds_read_b64_tr_b16 v[226:227], v192 offset:14336
	ds_read_b64_tr_b16 v[228:229], v192 offset:16384
	s_waitcnt lgkmcnt(0)
	v_mfma_f32_32x32x16_bf16 v[32:47], v[80:83], v[202:205], v[32:47]
	ds_read_b64_tr_b16 v[202:203], v192 offset:2560
	ds_read_b64_tr_b16 v[204:205], v192 offset:4608
	v_mfma_f32_32x32x16_bf16 v[32:47], v[84:87], v[206:209], v[32:47]
	ds_read_b64_tr_b16 v[206:207], v192 offset:6656
	ds_read_b64_tr_b16 v[208:209], v192 offset:8704
	v_mfma_f32_32x32x16_bf16 v[32:47], v[88:91], v[222:225], v[32:47]
	ds_read_b64_tr_b16 v[222:223], v192 offset:10752
	ds_read_b64_tr_b16 v[224:225], v192 offset:12800
	v_mfma_f32_32x32x16_bf16 v[32:47], v[92:95], v[226:229], v[32:47]
	ds_read_b64_tr_b16 v[226:227], v192 offset:14848
	ds_read_b64_tr_b16 v[228:229], v192 offset:16896
	s_waitcnt lgkmcnt(0)
	v_mfma_f32_32x32x16_bf16 v[16:31], v[80:83], v[202:205], v[16:31]
	v_max_f32_e32 v80, v96, v97
	v_max3_f32 v81, v64, v65, v66
	v_max3_f32 v80, v80, v98, v99
	v_max3_f32 v81, v81, v67, v68
	v_max3_f32 v80, v80, v100, v101
	v_mfma_f32_32x32x16_bf16 v[16:31], v[84:87], v[206:209], v[16:31]
	v_max3_f32 v81, v81, v69, v70
	v_max3_f32 v80, v80, v102, v103
	v_max3_f32 v81, v81, v71, v72
	v_max3_f32 v80, v80, v104, v105
	v_max3_f32 v81, v81, v73, v74
	v_max3_f32 v80, v80, v106, v107
	v_max3_f32 v81, v81, v75, v76
	v_mfma_f32_32x32x16_bf16 v[16:31], v[88:91], v[222:225], v[16:31]
	v_max3_f32 v80, v80, v108, v109
	v_max3_f32 v81, v81, v77, v78
	v_max3_f32 v80, v80, v110, v111
	v_max3_f32 v80, v80, v81, v79
	v_mov_b32_e32 v197, 1.0
	v_mfma_f32_32x32x16_bf16 v[16:31], v[92:95], v[226:229], v[16:31]
	v_cmp_ge_f32_e64 s[0:1], s56, v80
	s_cmp_eq_u64 s[0:1], exec
	s_cbranch_scc1 .Lc1_799
	s_branch .Lc1_802

.Lc1_799:
	v_exp_f32_e32 v159, v96
	v_exp_f32_e32 v161, v97
	v_exp_f32_e32 v157, v98
	v_exp_f32_e32 v160, v99
	v_exp_f32_e32 v155, v100
	v_exp_f32_e32 v158, v101
	v_exp_f32_e32 v154, v102
	v_exp_f32_e32 v156, v103
	v_exp_f32_e32 v151, v104
	v_exp_f32_e32 v153, v105
	v_exp_f32_e32 v149, v106
	v_exp_f32_e32 v152, v107
	v_exp_f32_e32 v147, v108
	v_exp_f32_e32 v150, v109
	v_exp_f32_e32 v146, v110
	v_exp_f32_e32 v148, v111
	v_fma_f32 v80, v193, v179, v195
	v_fma_f32 v179, v80, v198, v199
	s_cmp_gt_u32 s55, 32
	s_waitcnt vmcnt(4) lgkmcnt(0)
	s_barrier
	s_cbranch_scc1 .LBB0_803
	s_add_i32 s55, s55, 2
	v_mov_b32_e32 v193, v197
	ds_read_b128 v[80:83], v134 offset:50176
	ds_read_b128 v[84:87], v134 offset:58368
	ds_read_b128 v[196:199], v135 offset:50176
	ds_read_b128 v[200:203], v135 offset:58368
	s_waitcnt lgkmcnt(2)
	v_mfma_f32_32x32x16_bf16 v[96:111], v[80:83], v[122:125], 0
	v_exp_f32_e32 v204, v72
	v_exp_f32_e32 v205, v73
	v_exp_f32_e32 v206, v74
	v_exp_f32_e32 v207, v75
	v_exp_f32_e32 v208, v76
	v_exp_f32_e32 v209, v77
	v_mfma_f32_32x32x16_bf16 v[80:95], v[84:87], v[122:125], 0
	v_exp_f32_e32 v210, v78
	v_exp_f32_e32 v79, v79
	s_waitcnt lgkmcnt(0)
	v_mfma_f32_32x32x16_bf16 v[96:111], v[196:199], v[126:129], v[96:111]
	v_mfma_f32_32x32x16_bf16 v[80:95], v[200:203], v[126:129], v[80:95]
	ds_read_b128 v[196:199], v136 offset:50176
	ds_read_b128 v[200:203], v136 offset:58368
	s_waitcnt lgkmcnt(0)
	v_mfma_f32_32x32x16_bf16 v[96:111], v[196:199], v[118:121], v[96:111]
	v_mfma_f32_32x32x16_bf16 v[80:95], v[200:203], v[118:121], v[80:95]
	ds_read_b128 v[196:199], v137 offset:50176
	ds_read_b128 v[200:203], v137 offset:58368
	v_exp_f32_e32 v180, v64
	v_add_f32_e32 v64, v161, v159
	v_add_f32_e32 v195, v157, v160
	v_add_f32_e32 v64, v155, v64
	v_add_f32_e32 v195, v158, v195
	v_add_f32_e32 v64, v154, v64
	v_add_f32_e32 v195, v156, v195
	v_add_f32_e32 v64, v151, v64
	v_add_f32_e32 v195, v153, v195
	v_add_f32_e32 v64, v149, v64
	v_add_f32_e32 v195, v152, v195
	v_add_f32_e32 v64, v147, v64
	s_waitcnt lgkmcnt(0)
	v_mfma_f32_32x32x16_bf16 v[96:111], v[196:199], v[114:117], v[96:111]
	v_exp_f32_e32 v197, v65
	v_add_f32_e32 v195, v150, v195
	v_exp_f32_e32 v198, v66
	v_add_f32_e32 v64, v146, v64
	v_exp_f32_e32 v199, v67
	v_add_f32_e32 v195, v148, v195
	v_add_f32_e32 v64, v180, v64
	v_mfma_f32_32x32x16_bf16 v[80:95], v[200:203], v[114:117], v[80:95]
	v_exp_f32_e32 v200, v68
	v_exp_f32_e32 v201, v69
	v_add_f32_e32 v195, v197, v195
	v_exp_f32_e32 v202, v70
	v_add_f32_e32 v64, v198, v64
	v_exp_f32_e32 v203, v71
	v_add_f32_e32 v195, v199, v195
	v_add_f32_e32 v64, v200, v64
	v_add_f32_e32 v195, v201, v195
	v_add_f32_e32 v64, v202, v64
	v_add_f32_e32 v195, v203, v195
	v_add_f32_e32 v64, v204, v64
	v_add_f32_e32 v195, v205, v195
	v_add_f32_e32 v64, v206, v64
	v_add_f32_e32 v195, v207, v195
	v_add_f32_e32 v64, v208, v64
	v_add_f32_e32 v195, v209, v195
	v_add_f32_e32 v64, v210, v64
	v_add_f32_e32 v195, v79, v195
	v_add_f32_e32 v195, v195, v64
	v_cvt_pk_bf16_f32 v64, v159, v161
	v_cvt_pk_bf16_f32 v65, v157, v160
	v_cvt_pk_bf16_f32 v66, v155, v158
	v_cvt_pk_bf16_f32 v67, v154, v156
	v_cvt_pk_bf16_f32 v68, v151, v153
	v_cvt_pk_bf16_f32 v69, v149, v152
	v_cvt_pk_bf16_f32 v70, v147, v150
	v_cvt_pk_bf16_f32 v71, v146, v148
	v_cvt_pk_bf16_f32 v72, v180, v197
	v_cvt_pk_bf16_f32 v73, v198, v199
	v_cvt_pk_bf16_f32 v74, v200, v201
	v_cvt_pk_bf16_f32 v75, v202, v203
	v_cvt_pk_bf16_f32 v76, v204, v205
	v_cvt_pk_bf16_f32 v77, v206, v207
	v_cvt_pk_bf16_f32 v78, v208, v209
	v_cvt_pk_bf16_f32 v79, v210, v79
	s_add_i32 m0, s84, 0x400
	s_add_u32 s66, s78, s65
	s_addc_u32 s67, s79, 0
	global_load_lds_dwordx4 v185, s[66:67]
	s_add_i32 m0, s84, 0x2400
	s_add_i32 s64, s65, 0x60000
	global_load_lds_dwordx4 v184, s[66:67]
	s_add_i32 m0, s84, 0x10400
	s_add_u32 s70, s80, s64
	s_addc_u32 s71, s81, 0
	global_load_lds_dwordx4 v183, s[70:71]
	s_add_i32 m0, s84, 0x12400
	s_mov_b32 s65, s64
	global_load_lds_dwordx4 v182, s[70:71]
	ds_read_b64_tr_b16 v[198:199], v192 offset:17408
	ds_read_b64_tr_b16 v[200:201], v192 offset:19456
	ds_read_b64_tr_b16 v[202:203], v192 offset:21504
	ds_read_b64_tr_b16 v[204:205], v192 offset:23552
	ds_read_b64_tr_b16 v[206:207], v192 offset:25600
	ds_read_b64_tr_b16 v[208:209], v192 offset:27648
	ds_read_b64_tr_b16 v[222:223], v192 offset:29696
	ds_read_b64_tr_b16 v[224:225], v192 offset:31744
	s_waitcnt lgkmcnt(0)
	v_mfma_f32_32x32x16_bf16 v[0:15], v[64:67], v[198:201], v[0:15]
	ds_read_b64_tr_b16 v[198:199], v192 offset:17920
	ds_read_b64_tr_b16 v[200:201], v192 offset:19968
	v_mfma_f32_32x32x16_bf16 v[0:15], v[68:71], v[202:205], v[0:15]
	ds_read_b64_tr_b16 v[202:203], v192 offset:22016
	ds_read_b64_tr_b16 v[204:205], v192 offset:24064
	v_mfma_f32_32x32x16_bf16 v[0:15], v[72:75], v[206:209], v[0:15]
	ds_read_b64_tr_b16 v[206:207], v192 offset:26112
	ds_read_b64_tr_b16 v[208:209], v192 offset:28160
	v_mfma_f32_32x32x16_bf16 v[0:15], v[76:79], v[222:225], v[0:15]
	ds_read_b64_tr_b16 v[222:223], v192 offset:30208
	ds_read_b64_tr_b16 v[224:225], v192 offset:32256
	s_waitcnt lgkmcnt(0)
	v_mfma_f32_32x32x16_bf16 v[48:63], v[64:67], v[198:201], v[48:63]
	ds_read_b64_tr_b16 v[198:199], v192 offset:18432
	ds_read_b64_tr_b16 v[200:201], v192 offset:20480
	v_mfma_f32_32x32x16_bf16 v[48:63], v[68:71], v[202:205], v[48:63]
	ds_read_b64_tr_b16 v[202:203], v192 offset:22528
	ds_read_b64_tr_b16 v[204:205], v192 offset:24576
	v_mfma_f32_32x32x16_bf16 v[48:63], v[72:75], v[206:209], v[48:63]
	ds_read_b64_tr_b16 v[206:207], v192 offset:26624
	ds_read_b64_tr_b16 v[208:209], v192 offset:28672
	v_mfma_f32_32x32x16_bf16 v[48:63], v[76:79], v[222:225], v[48:63]
	ds_read_b64_tr_b16 v[222:223], v192 offset:30720
	ds_read_b64_tr_b16 v[224:225], v192 offset:32768
	s_waitcnt lgkmcnt(0)
	v_mfma_f32_32x32x16_bf16 v[32:47], v[64:67], v[198:201], v[32:47]
	ds_read_b64_tr_b16 v[198:199], v192 offset:18944
	ds_read_b64_tr_b16 v[200:201], v192 offset:20992
	v_mfma_f32_32x32x16_bf16 v[32:47], v[68:71], v[202:205], v[32:47]
	ds_read_b64_tr_b16 v[202:203], v192 offset:23040
	ds_read_b64_tr_b16 v[204:205], v192 offset:25088
	v_mfma_f32_32x32x16_bf16 v[32:47], v[72:75], v[206:209], v[32:47]
	ds_read_b64_tr_b16 v[206:207], v192 offset:27136
	ds_read_b64_tr_b16 v[208:209], v192 offset:29184
	v_mfma_f32_32x32x16_bf16 v[32:47], v[76:79], v[222:225], v[32:47]
	ds_read_b64_tr_b16 v[222:223], v192 offset:31232
	ds_read_b64_tr_b16 v[224:225], v192 offset:33280
	s_waitcnt lgkmcnt(0)
	v_mfma_f32_32x32x16_bf16 v[16:31], v[64:67], v[198:201], v[16:31]
	v_max_f32_e32 v64, v96, v97
	v_max3_f32 v65, v80, v81, v82
	v_max3_f32 v64, v64, v98, v99
	v_max3_f32 v65, v65, v83, v84
	v_max3_f32 v64, v64, v100, v101
	v_mfma_f32_32x32x16_bf16 v[16:31], v[68:71], v[202:205], v[16:31]
	v_max3_f32 v65, v65, v85, v86
	v_max3_f32 v64, v64, v102, v103
	v_max3_f32 v65, v65, v87, v88
	v_max3_f32 v64, v64, v104, v105
	v_max3_f32 v65, v65, v89, v90
	v_max3_f32 v64, v64, v106, v107
	v_max3_f32 v65, v65, v91, v92
	v_mfma_f32_32x32x16_bf16 v[16:31], v[72:75], v[206:209], v[16:31]
	v_max3_f32 v64, v64, v108, v109
	v_max3_f32 v65, v65, v93, v94
	v_max3_f32 v64, v64, v110, v111
	v_max3_f32 v64, v64, v65, v95
	v_mov_b32_e32 v198, 1.0
	v_mfma_f32_32x32x16_bf16 v[16:31], v[76:79], v[222:225], v[16:31]
	v_cmp_ge_f32_e64 s[0:1], s56, v64
	s_cmp_eq_u64 s[0:1], exec
	s_cbranch_scc1 .Lc2_792
	s_branch .Lc2_801

.Lc2_792:
	v_exp_f32_e32 v197, v96
	v_exp_f32_e32 v208, v97
	v_exp_f32_e32 v209, v98
	v_exp_f32_e32 v210, v99
	v_exp_f32_e32 v211, v100
	v_exp_f32_e32 v220, v101
	v_exp_f32_e32 v221, v102
	v_exp_f32_e32 v222, v103
	v_exp_f32_e32 v223, v104
	v_exp_f32_e32 v224, v105
	v_exp_f32_e32 v225, v106
	v_exp_f32_e32 v226, v107
	v_exp_f32_e32 v227, v108
	v_exp_f32_e32 v228, v109
	v_exp_f32_e32 v229, v110
	v_exp_f32_e32 v230, v111
	s_waitcnt vmcnt(4) lgkmcnt(0)
	s_barrier
	ds_read_b128 v[64:67], v130 offset:50176
	ds_read_b128 v[68:71], v130 offset:58368
	ds_read_b128 v[200:203], v131 offset:50176
	ds_read_b128 v[204:207], v131 offset:58368
	v_exp_f32_e32 v231, v87
	s_waitcnt lgkmcnt(2)
	v_mfma_f32_32x32x16_bf16 v[96:111], v[64:67], v[122:125], 0
	v_exp_f32_e32 v232, v88
	v_exp_f32_e32 v233, v89
	v_exp_f32_e32 v234, v90
	v_exp_f32_e32 v235, v91
	v_exp_f32_e32 v236, v92
	v_exp_f32_e32 v237, v93
	v_exp_f32_e32 v238, v94
	v_mfma_f32_32x32x16_bf16 v[64:79], v[68:71], v[122:125], 0
	v_exp_f32_e32 v95, v95
	s_waitcnt lgkmcnt(0)
	v_mfma_f32_32x32x16_bf16 v[96:111], v[200:203], v[126:129], v[96:111]
	v_mfma_f32_32x32x16_bf16 v[64:79], v[204:207], v[126:129], v[64:79]
	ds_read_b128 v[200:203], v132 offset:50176
	ds_read_b128 v[204:207], v132 offset:58368
	s_waitcnt lgkmcnt(0)
	v_mfma_f32_32x32x16_bf16 v[96:111], v[200:203], v[118:121], v[96:111]
	v_mfma_f32_32x32x16_bf16 v[64:79], v[204:207], v[118:121], v[64:79]
	ds_read_b128 v[200:203], v133 offset:50176
	ds_read_b128 v[204:207], v133 offset:58368
	s_waitcnt lgkmcnt(0)
	v_mfma_f32_32x32x16_bf16 v[96:111], v[200:203], v[114:117], v[96:111]
	v_exp_f32_e32 v201, v80
	v_add_f32_e32 v80, v208, v197
	v_add_f32_e32 v199, v209, v210
	v_add_f32_e32 v80, v211, v80
	v_add_f32_e32 v199, v220, v199
	v_add_f32_e32 v80, v221, v80
	v_add_f32_e32 v199, v222, v199
	v_add_f32_e32 v80, v223, v80
	v_add_f32_e32 v199, v224, v199
	v_add_f32_e32 v80, v225, v80
	v_add_f32_e32 v199, v226, v199
	v_add_f32_e32 v80, v227, v80
	v_exp_f32_e32 v202, v81
	v_add_f32_e32 v199, v228, v199
	v_exp_f32_e32 v203, v82
	v_add_f32_e32 v80, v229, v80
	v_mfma_f32_32x32x16_bf16 v[64:79], v[204:207], v[114:117], v[64:79]
	v_exp_f32_e32 v204, v83
	v_add_f32_e32 v199, v230, v199
	v_exp_f32_e32 v205, v84
	v_add_f32_e32 v80, v201, v80
	v_exp_f32_e32 v206, v85
	v_add_f32_e32 v199, v202, v199
	v_exp_f32_e32 v207, v86
	v_add_f32_e32 v80, v203, v80
	v_add_f32_e32 v199, v204, v199
	v_add_f32_e32 v80, v205, v80
	v_add_f32_e32 v199, v206, v199
	v_add_f32_e32 v80, v207, v80
	v_add_f32_e32 v199, v231, v199
	v_add_f32_e32 v80, v232, v80
	v_add_f32_e32 v199, v233, v199
	v_add_f32_e32 v80, v234, v80
	v_add_f32_e32 v199, v235, v199
	v_add_f32_e32 v80, v236, v80
	v_add_f32_e32 v199, v237, v199
	v_add_f32_e32 v80, v238, v80
	v_add_f32_e32 v199, v95, v199
	v_add_f32_e32 v199, v199, v80
	v_cvt_pk_bf16_f32 v80, v197, v208
	v_cvt_pk_bf16_f32 v81, v209, v210
	v_cvt_pk_bf16_f32 v82, v211, v220
	v_cvt_pk_bf16_f32 v83, v221, v222
	v_cvt_pk_bf16_f32 v84, v223, v224
	v_cvt_pk_bf16_f32 v85, v225, v226
	v_cvt_pk_bf16_f32 v86, v227, v228
	v_cvt_pk_bf16_f32 v87, v229, v230
	v_cvt_pk_bf16_f32 v88, v201, v202
	v_cvt_pk_bf16_f32 v89, v203, v204
	v_cvt_pk_bf16_f32 v90, v205, v206
	v_cvt_pk_bf16_f32 v91, v207, v231
	v_cvt_pk_bf16_f32 v92, v232, v233
	v_cvt_pk_bf16_f32 v93, v234, v235
	v_cvt_pk_bf16_f32 v94, v236, v237
	v_cvt_pk_bf16_f32 v95, v238, v95
	s_add_i32 m0, s84, 0x4400
	s_add_u32 s66, s78, s65
	s_addc_u32 s67, s79, 0
	global_load_lds_dwordx4 v185, s[66:67]
	s_add_i32 m0, s84, 0x6400
	s_add_i32 s64, s65, 0x60000
	global_load_lds_dwordx4 v184, s[66:67]
	s_cmp_eq_u32 s55, 29
	s_cselect_b32 s64, s89, s64
	s_add_i32 m0, s84, 0x14400
	s_add_u32 s70, s80, s64
	s_addc_u32 s71, s81, 0
	global_load_lds_dwordx4 v183, s[70:71]
	s_add_i32 m0, s84, 0x16400
	s_mov_b32 s65, s64
	global_load_lds_dwordx4 v182, s[70:71]
.Lc2_794:
	ds_read_b64_tr_b16 v[202:203], v192 offset:33792
	ds_read_b64_tr_b16 v[204:205], v192 offset:35840
	ds_read_b64_tr_b16 v[206:207], v192 offset:37888
	ds_read_b64_tr_b16 v[208:209], v192 offset:39936
	ds_read_b64_tr_b16 v[222:223], v192 offset:41984
	ds_read_b64_tr_b16 v[224:225], v192 offset:44032
	ds_read_b64_tr_b16 v[226:227], v192 offset:46080
	ds_read_b64_tr_b16 v[228:229], v192 offset:48128
	s_waitcnt lgkmcnt(0)
	v_mfma_f32_32x32x16_bf16 v[0:15], v[80:83], v[202:205], v[0:15]
	ds_read_b64_tr_b16 v[202:203], v192 offset:34304
	ds_read_b64_tr_b16 v[204:205], v192 offset:36352
	v_mfma_f32_32x32x16_bf16 v[0:15], v[84:87], v[206:209], v[0:15]
	ds_read_b64_tr_b16 v[206:207], v192 offset:38400
	ds_read_b64_tr_b16 v[208:209], v192 offset:40448
	v_mfma_f32_32x32x16_bf16 v[0:15], v[88:91], v[222:225], v[0:15]
	ds_read_b64_tr_b16 v[222:223], v192 offset:42496
	ds_read_b64_tr_b16 v[224:225], v192 offset:44544
	v_mfma_f32_32x32x16_bf16 v[0:15], v[92:95], v[226:229], v[0:15]
	ds_read_b64_tr_b16 v[226:227], v192 offset:46592
	ds_read_b64_tr_b16 v[228:229], v192 offset:48640
	s_waitcnt lgkmcnt(0)
	v_mfma_f32_32x32x16_bf16 v[48:63], v[80:83], v[202:205], v[48:63]
	ds_read_b64_tr_b16 v[202:203], v192 offset:34816
	ds_read_b64_tr_b16 v[204:205], v192 offset:36864
	v_mfma_f32_32x32x16_bf16 v[48:63], v[84:87], v[206:209], v[48:63]
	ds_read_b64_tr_b16 v[206:207], v192 offset:38912
	ds_read_b64_tr_b16 v[208:209], v192 offset:40960
	v_mfma_f32_32x32x16_bf16 v[48:63], v[88:91], v[222:225], v[48:63]
	ds_read_b64_tr_b16 v[222:223], v192 offset:43008
	ds_read_b64_tr_b16 v[224:225], v192 offset:45056
	v_mfma_f32_32x32x16_bf16 v[48:63], v[92:95], v[226:229], v[48:63]
	ds_read_b64_tr_b16 v[226:227], v192 offset:47104
	ds_read_b64_tr_b16 v[228:229], v192 offset:49152
	s_waitcnt lgkmcnt(0)
	v_mfma_f32_32x32x16_bf16 v[32:47], v[80:83], v[202:205], v[32:47]
	ds_read_b64_tr_b16 v[202:203], v192 offset:35328
	ds_read_b64_tr_b16 v[204:205], v192 offset:37376
	v_mfma_f32_32x32x16_bf16 v[32:47], v[84:87], v[206:209], v[32:47]
	ds_read_b64_tr_b16 v[206:207], v192 offset:39424
	ds_read_b64_tr_b16 v[208:209], v192 offset:41472
	v_mfma_f32_32x32x16_bf16 v[32:47], v[88:91], v[222:225], v[32:47]
	ds_read_b64_tr_b16 v[222:223], v192 offset:43520
	ds_read_b64_tr_b16 v[224:225], v192 offset:45568
	v_mfma_f32_32x32x16_bf16 v[32:47], v[92:95], v[226:229], v[32:47]
	ds_read_b64_tr_b16 v[226:227], v192 offset:47616
	ds_read_b64_tr_b16 v[228:229], v192 offset:49664
	s_waitcnt lgkmcnt(0)
	v_mfma_f32_32x32x16_bf16 v[16:31], v[80:83], v[202:205], v[16:31]
	v_max_f32_e32 v80, v96, v97
	v_max3_f32 v81, v64, v65, v66
	v_max3_f32 v80, v80, v98, v99
	v_max3_f32 v81, v81, v67, v68
	v_max3_f32 v80, v80, v100, v101
	v_mfma_f32_32x32x16_bf16 v[16:31], v[84:87], v[206:209], v[16:31]
	v_max3_f32 v81, v81, v69, v70
	v_max3_f32 v80, v80, v102, v103
	v_max3_f32 v81, v81, v71, v72
	v_max3_f32 v80, v80, v104, v105
	v_max3_f32 v81, v81, v73, v74
	v_max3_f32 v80, v80, v106, v107
	v_max3_f32 v81, v81, v75, v76
	v_mfma_f32_32x32x16_bf16 v[16:31], v[88:91], v[222:225], v[16:31]
	v_max3_f32 v80, v80, v108, v109
	v_max3_f32 v81, v81, v77, v78
	v_max3_f32 v80, v80, v110, v111
	v_max3_f32 v80, v80, v81, v79
	v_mov_b32_e32 v197, 1.0
	v_mfma_f32_32x32x16_bf16 v[16:31], v[92:95], v[226:229], v[16:31]
	v_cmp_ge_f32_e64 s[0:1], s56, v80
	s_cmp_eq_u64 s[0:1], exec
	s_cbranch_scc1 .Lc2_799
	s_branch .Lc2_802

.Lc2_799:
	v_exp_f32_e32 v159, v96
	v_exp_f32_e32 v161, v97
	v_exp_f32_e32 v157, v98
	v_exp_f32_e32 v160, v99
	v_exp_f32_e32 v155, v100
	v_exp_f32_e32 v158, v101
	v_exp_f32_e32 v154, v102
	v_exp_f32_e32 v156, v103
	v_exp_f32_e32 v151, v104
	v_exp_f32_e32 v153, v105
	v_exp_f32_e32 v149, v106
	v_exp_f32_e32 v152, v107
	v_exp_f32_e32 v147, v108
	v_exp_f32_e32 v150, v109
	v_exp_f32_e32 v146, v110
	v_exp_f32_e32 v148, v111
	v_fma_f32 v80, v193, v179, v195
	v_fma_f32 v179, v80, v198, v199
	s_cmp_gt_u32 s55, 32
	s_waitcnt vmcnt(4) lgkmcnt(0)
	s_barrier
	s_cbranch_scc1 .LBB0_803
	s_add_i32 s55, s55, 2
	v_mov_b32_e32 v193, v197
	s_branch .LBB0_787

.LBB0_802:
	v_mov_b32_e32 v81, v80
	s_nop 1
	v_permlane32_swap_b32_e32 v80, v81
	v_max_f32_e32 v80, v80, v81
	v_sub_f32_e32 v81, v80, v164
	v_cmp_lt_f32_e32 vcc, s75, v81
	v_max_f32_e32 v80, v80, v80
	v_max_f32_e32 v81, v164, v164
	v_max_f32_e32 v80, v81, v80
	v_cndmask_b32_e32 v80, v164, v80, vcc
	v_sub_f32_e32 v81, v164, v80
	v_exp_f32_e32 v197, v81
	v_pk_add_f32 v[96:97], v[96:97], v[80:81] op_sel_hi:[1,0] neg_lo:[0,1] neg_hi:[0,1]
	v_pk_add_f32 v[98:99], v[98:99], v[80:81] op_sel_hi:[1,0] neg_lo:[0,1] neg_hi:[0,1]
	v_pk_add_f32 v[100:101], v[100:101], v[80:81] op_sel_hi:[1,0] neg_lo:[0,1] neg_hi:[0,1]
	v_pk_add_f32 v[102:103], v[102:103], v[80:81] op_sel_hi:[1,0] neg_lo:[0,1] neg_hi:[0,1]
	v_pk_add_f32 v[104:105], v[104:105], v[80:81] op_sel_hi:[1,0] neg_lo:[0,1] neg_hi:[0,1]
	v_pk_add_f32 v[106:107], v[106:107], v[80:81] op_sel_hi:[1,0] neg_lo:[0,1] neg_hi:[0,1]
	v_pk_add_f32 v[108:109], v[108:109], v[80:81] op_sel_hi:[1,0] neg_lo:[0,1] neg_hi:[0,1]
	v_pk_add_f32 v[110:111], v[110:111], v[80:81] op_sel_hi:[1,0] neg_lo:[0,1] neg_hi:[0,1]
	v_sub_f32_e32 v79, v79, v80
	v_sub_f32_e32 v78, v78, v80
	v_sub_f32_e32 v77, v77, v80
	v_sub_f32_e32 v76, v76, v80
	v_sub_f32_e32 v75, v75, v80
	v_sub_f32_e32 v74, v74, v80
	v_sub_f32_e32 v73, v73, v80
	v_sub_f32_e32 v72, v72, v80
	v_sub_f32_e32 v71, v71, v80
	v_sub_f32_e32 v70, v70, v80
	v_sub_f32_e32 v69, v69, v80
	v_sub_f32_e32 v68, v68, v80
	v_sub_f32_e32 v67, v67, v80
	v_sub_f32_e32 v66, v66, v80
	v_sub_f32_e32 v65, v65, v80
	v_sub_f32_e32 v64, v64, v80
	v_mov_b32_e32 v164, v80
	s_mov_b32 s56, 0xff800000
	s_branch .LBB0_795
.Lc1_801:
	v_mov_b32_e32 v65, v64
	s_nop 1
	v_permlane32_swap_b32_e32 v64, v65
	v_max_f32_e32 v64, v64, v65
	v_sub_f32_e32 v65, v64, v164
	v_cmp_lt_f32_e32 vcc, s75, v65
	v_max_f32_e32 v64, v64, v64
	v_max_f32_e32 v65, v164, v164
	v_max_f32_e32 v64, v65, v64
	v_cndmask_b32_e32 v64, v164, v64, vcc
	v_sub_f32_e32 v65, v164, v64
	v_exp_f32_e32 v198, v65
	v_pk_add_f32 v[96:97], v[96:97], v[64:65] op_sel_hi:[1,0] neg_lo:[0,1] neg_hi:[0,1]
	v_pk_add_f32 v[98:99], v[98:99], v[64:65] op_sel_hi:[1,0] neg_lo:[0,1] neg_hi:[0,1]
	v_pk_add_f32 v[100:101], v[100:101], v[64:65] op_sel_hi:[1,0] neg_lo:[0,1] neg_hi:[0,1]
	v_pk_add_f32 v[102:103], v[102:103], v[64:65] op_sel_hi:[1,0] neg_lo:[0,1] neg_hi:[0,1]
	v_pk_add_f32 v[104:105], v[104:105], v[64:65] op_sel_hi:[1,0] neg_lo:[0,1] neg_hi:[0,1]
	v_pk_add_f32 v[106:107], v[106:107], v[64:65] op_sel_hi:[1,0] neg_lo:[0,1] neg_hi:[0,1]
	v_pk_add_f32 v[108:109], v[108:109], v[64:65] op_sel_hi:[1,0] neg_lo:[0,1] neg_hi:[0,1]
	v_pk_add_f32 v[110:111], v[110:111], v[64:65] op_sel_hi:[1,0] neg_lo:[0,1] neg_hi:[0,1]
	v_sub_f32_e32 v95, v95, v64
	v_sub_f32_e32 v94, v94, v64
	v_sub_f32_e32 v93, v93, v64
	v_sub_f32_e32 v92, v92, v64
	v_sub_f32_e32 v91, v91, v64
	v_sub_f32_e32 v90, v90, v64
	v_sub_f32_e32 v89, v89, v64
	v_sub_f32_e32 v88, v88, v64
	v_sub_f32_e32 v87, v87, v64
	v_sub_f32_e32 v86, v86, v64
	v_sub_f32_e32 v85, v85, v64
	v_sub_f32_e32 v84, v84, v64
	v_sub_f32_e32 v83, v83, v64
	v_sub_f32_e32 v82, v82, v64
	v_sub_f32_e32 v81, v81, v64
	v_sub_f32_e32 v80, v80, v64
	v_mov_b32_e32 v164, v64
	s_mov_b32 s56, 0xff800000
	s_branch .Lc1_788
.Lc1_802:
	v_mov_b32_e32 v81, v80
	s_nop 1
	v_permlane32_swap_b32_e32 v80, v81
	v_max_f32_e32 v80, v80, v81
	v_sub_f32_e32 v81, v80, v164
	v_cmp_lt_f32_e32 vcc, s75, v81
	v_max_f32_e32 v80, v80, v80
	v_max_f32_e32 v81, v164, v164
	v_max_f32_e32 v80, v81, v80
	v_cndmask_b32_e32 v80, v164, v80, vcc
	v_sub_f32_e32 v81, v164, v80
	v_exp_f32_e32 v197, v81
	v_pk_add_f32 v[96:97], v[96:97], v[80:81] op_sel_hi:[1,0] neg_lo:[0,1] neg_hi:[0,1]
	v_pk_add_f32 v[98:99], v[98:99], v[80:81] op_sel_hi:[1,0] neg_lo:[0,1] neg_hi:[0,1]
	v_pk_add_f32 v[100:101], v[100:101], v[80:81] op_sel_hi:[1,0] neg_lo:[0,1] neg_hi:[0,1]
	v_pk_add_f32 v[102:103], v[102:103], v[80:81] op_sel_hi:[1,0] neg_lo:[0,1] neg_hi:[0,1]
	v_pk_add_f32 v[104:105], v[104:105], v[80:81] op_sel_hi:[1,0] neg_lo:[0,1] neg_hi:[0,1]
	v_pk_add_f32 v[106:107], v[106:107], v[80:81] op_sel_hi:[1,0] neg_lo:[0,1] neg_hi:[0,1]
	v_pk_add_f32 v[108:109], v[108:109], v[80:81] op_sel_hi:[1,0] neg_lo:[0,1] neg_hi:[0,1]
	v_pk_add_f32 v[110:111], v[110:111], v[80:81] op_sel_hi:[1,0] neg_lo:[0,1] neg_hi:[0,1]
	v_sub_f32_e32 v79, v79, v80
	v_sub_f32_e32 v78, v78, v80
	v_sub_f32_e32 v77, v77, v80
	v_sub_f32_e32 v76, v76, v80
	v_sub_f32_e32 v75, v75, v80
	v_sub_f32_e32 v74, v74, v80
	v_sub_f32_e32 v73, v73, v80
	v_sub_f32_e32 v72, v72, v80
	v_sub_f32_e32 v71, v71, v80
	v_sub_f32_e32 v70, v70, v80
	v_sub_f32_e32 v69, v69, v80
	v_sub_f32_e32 v68, v68, v80
	v_sub_f32_e32 v67, v67, v80
	v_sub_f32_e32 v66, v66, v80
	v_sub_f32_e32 v65, v65, v80
	v_sub_f32_e32 v64, v64, v80
	v_mov_b32_e32 v164, v80
	s_mov_b32 s56, 0xff800000
	s_branch .Lc1_795
.Lc2_801:
	v_mov_b32_e32 v65, v64
	s_nop 1
	v_permlane32_swap_b32_e32 v64, v65
	v_max_f32_e32 v64, v64, v65
	v_sub_f32_e32 v65, v64, v164
	v_cmp_lt_f32_e32 vcc, s75, v65
	v_max_f32_e32 v64, v64, v64
	v_max_f32_e32 v65, v164, v164
	v_max_f32_e32 v64, v65, v64
	v_cndmask_b32_e32 v64, v164, v64, vcc
	v_sub_f32_e32 v65, v164, v64
	v_exp_f32_e32 v198, v65
	v_pk_add_f32 v[96:97], v[96:97], v[64:65] op_sel_hi:[1,0] neg_lo:[0,1] neg_hi:[0,1]
	v_pk_add_f32 v[98:99], v[98:99], v[64:65] op_sel_hi:[1,0] neg_lo:[0,1] neg_hi:[0,1]
	v_pk_add_f32 v[100:101], v[100:101], v[64:65] op_sel_hi:[1,0] neg_lo:[0,1] neg_hi:[0,1]
	v_pk_add_f32 v[102:103], v[102:103], v[64:65] op_sel_hi:[1,0] neg_lo:[0,1] neg_hi:[0,1]
	v_pk_add_f32 v[104:105], v[104:105], v[64:65] op_sel_hi:[1,0] neg_lo:[0,1] neg_hi:[0,1]
	v_pk_add_f32 v[106:107], v[106:107], v[64:65] op_sel_hi:[1,0] neg_lo:[0,1] neg_hi:[0,1]
	v_pk_add_f32 v[108:109], v[108:109], v[64:65] op_sel_hi:[1,0] neg_lo:[0,1] neg_hi:[0,1]
	v_pk_add_f32 v[110:111], v[110:111], v[64:65] op_sel_hi:[1,0] neg_lo:[0,1] neg_hi:[0,1]
	v_sub_f32_e32 v95, v95, v64
	v_sub_f32_e32 v94, v94, v64
	v_sub_f32_e32 v93, v93, v64
	v_sub_f32_e32 v92, v92, v64
	v_sub_f32_e32 v91, v91, v64
	v_sub_f32_e32 v90, v90, v64
	v_sub_f32_e32 v89, v89, v64
	v_sub_f32_e32 v88, v88, v64
	v_sub_f32_e32 v87, v87, v64
	v_sub_f32_e32 v86, v86, v64
	v_sub_f32_e32 v85, v85, v64
	v_sub_f32_e32 v84, v84, v64
	v_sub_f32_e32 v83, v83, v64
	v_sub_f32_e32 v82, v82, v64
	v_sub_f32_e32 v81, v81, v64
	v_sub_f32_e32 v80, v80, v64
	v_mov_b32_e32 v164, v64
	s_mov_b32 s56, 0xff800000
	s_branch .Lc2_788

.LBB0_803:
	s_waitcnt vmcnt(0)
	s_barrier
	v_add_u32_e32 v180, 0x8000, v194
	v_add_u32_e32 v134, s20, v189
	v_add_u32_e32 v84, v134, v190
	ds_read_b128 v[80:83], v84 offset:50176
	ds_read_b128 v[84:87], v84 offset:58368
	v_add_u32_e32 v130, v134, v188
	v_exp_f32_e32 v78, v78
	v_exp_f32_e32 v79, v79
	s_waitcnt lgkmcnt(1)
	v_mfma_f32_32x32x16_bf16 v[96:111], v[80:83], v[122:125], 0
	s_waitcnt lgkmcnt(0)
	v_mfma_f32_32x32x16_bf16 v[80:95], v[84:87], v[122:125], 0
	ds_read_b128 v[122:125], v130 offset:50176
	ds_read_b128 v[130:133], v130 offset:58368
	s_waitcnt lgkmcnt(1)
	v_mfma_f32_32x32x16_bf16 v[96:111], v[122:125], v[126:129], v[96:111]
	s_waitcnt lgkmcnt(0)
	v_mfma_f32_32x32x16_bf16 v[80:95], v[130:133], v[126:129], v[80:95]
	v_add_u32_e32 v126, v134, v187
	ds_read_b128 v[122:125], v126 offset:50176
	ds_read_b128 v[126:129], v126 offset:58368
	s_waitcnt lgkmcnt(1)
	v_mfma_f32_32x32x16_bf16 v[96:111], v[122:125], v[118:121], v[96:111]
	v_add_u32_e32 v122, v134, v186
	s_waitcnt lgkmcnt(0)
	v_mfma_f32_32x32x16_bf16 v[80:95], v[126:129], v[118:121], v[80:95]
	ds_read_b128 v[118:121], v122 offset:50176
	ds_read_b128 v[122:125], v122 offset:58368
	v_exp_f32_e32 v126, v76
	v_exp_f32_e32 v127, v77
	s_waitcnt lgkmcnt(1)
	v_mfma_f32_32x32x16_bf16 v[96:111], v[118:121], v[114:117], v[96:111]
	v_exp_f32_e32 v118, v68
	v_exp_f32_e32 v119, v69
	v_exp_f32_e32 v120, v70
	v_exp_f32_e32 v121, v71
	s_waitcnt lgkmcnt(0)
	v_mfma_f32_32x32x16_bf16 v[80:95], v[122:125], v[114:117], v[80:95]
	v_exp_f32_e32 v114, v64
	v_add_f32_e32 v64, 0, v159
	v_add_f32_e32 v64, v161, v64
	v_add_f32_e32 v64, v157, v64
	v_add_f32_e32 v64, v160, v64
	v_add_f32_e32 v64, v155, v64
	v_add_f32_e32 v64, v158, v64
	v_add_f32_e32 v64, v154, v64
	v_add_f32_e32 v64, v156, v64
	v_add_f32_e32 v64, v151, v64
	v_add_f32_e32 v64, v153, v64
	v_add_f32_e32 v64, v149, v64
	v_add_f32_e32 v64, v152, v64
	v_add_f32_e32 v64, v147, v64
	v_exp_f32_e32 v115, v65
	v_add_f32_e32 v64, v150, v64
	v_exp_f32_e32 v116, v66
	v_add_f32_e32 v64, v146, v64
	v_exp_f32_e32 v117, v67
	v_add_f32_e32 v64, v148, v64
	v_add_f32_e32 v64, v114, v64
	v_add_f32_e32 v64, v115, v64
	v_add_f32_e32 v64, v116, v64
	v_add_f32_e32 v64, v117, v64
	v_exp_f32_e32 v122, v72
	v_add_f32_e32 v64, v118, v64
	v_exp_f32_e32 v123, v73
	v_add_f32_e32 v64, v119, v64
	v_exp_f32_e32 v124, v74
	v_add_f32_e32 v64, v120, v64
	v_exp_f32_e32 v125, v75
	v_add_f32_e32 v64, v121, v64
	v_add_f32_e32 v64, v122, v64
	v_add_f32_e32 v64, v123, v64
	v_add_f32_e32 v64, v124, v64
	v_add_f32_e32 v64, v125, v64
	v_add_f32_e32 v64, v126, v64
	v_add_f32_e32 v64, v127, v64
	v_add_f32_e32 v64, v78, v64
	v_add_f32_e32 v64, v79, v64
	v_cvt_pk_bf16_f32 v66, v159, v161
	v_cvt_pk_bf16_f32 v67, v157, v160
	v_cvt_pk_bf16_f32 v68, v155, v158
	v_cvt_pk_bf16_f32 v69, v154, v156
	v_cvt_pk_bf16_f32 v70, v151, v153
	v_cvt_pk_bf16_f32 v71, v149, v152
	v_cvt_pk_bf16_f32 v72, v147, v150
	v_cvt_pk_bf16_f32 v73, v146, v148
	v_cvt_pk_bf16_f32 v74, v114, v115
	v_cvt_pk_bf16_f32 v75, v116, v117
	v_cvt_pk_bf16_f32 v76, v118, v119
	v_cvt_pk_bf16_f32 v77, v120, v121
	v_cvt_pk_bf16_f32 v114, v122, v123
	v_cvt_pk_bf16_f32 v115, v124, v125
	v_cvt_pk_bf16_f32 v116, v126, v127
	v_cvt_pk_bf16_f32 v117, v78, v79
	s_nop 0
	s_add_i32 s0, 0, 0x4400
	v_add_u32_e32 v78, s0, v192
	ds_read_b64_tr_b16 v[118:119], v78 offset:0
	ds_read_b64_tr_b16 v[120:121], v78 offset:0x800
	ds_read_b64_tr_b16 v[122:123], v78 offset:0x1000
	ds_read_b64_tr_b16 v[124:125], v78 offset:0x1800
	ds_read_b64_tr_b16 v[126:127], v78 offset:0x2000
	ds_read_b64_tr_b16 v[128:129], v78 offset:0x2800
	ds_read_b64_tr_b16 v[130:131], v78 offset:0x3000
	ds_read_b64_tr_b16 v[132:133], v78 offset:0x3800
	s_waitcnt lgkmcnt(0)
	s_nop 0
	v_mfma_f32_32x32x16_bf16 v[0:15], v[66:69], v[118:121], v[0:15]
	ds_read_b64_tr_b16 v[118:119], v78 offset:0x200
	ds_read_b64_tr_b16 v[120:121], v78 offset:0xa00
	v_mfma_f32_32x32x16_bf16 v[0:15], v[70:73], v[122:125], v[0:15]
	ds_read_b64_tr_b16 v[122:123], v78 offset:0x1200
	ds_read_b64_tr_b16 v[124:125], v78 offset:0x1a00
	v_mfma_f32_32x32x16_bf16 v[0:15], v[74:77], v[126:129], v[0:15]
	ds_read_b64_tr_b16 v[126:127], v78 offset:0x2200
	ds_read_b64_tr_b16 v[128:129], v78 offset:0x2a00
	v_mfma_f32_32x32x16_bf16 v[0:15], v[114:117], v[130:133], v[0:15]
	ds_read_b64_tr_b16 v[130:131], v78 offset:0x3200
	ds_read_b64_tr_b16 v[132:133], v78 offset:0x3a00
	s_waitcnt lgkmcnt(0)
	v_mfma_f32_32x32x16_bf16 v[48:63], v[66:69], v[118:121], v[48:63]
	ds_read_b64_tr_b16 v[118:119], v78 offset:0x400
	ds_read_b64_tr_b16 v[120:121], v78 offset:0xc00
	v_mfma_f32_32x32x16_bf16 v[48:63], v[70:73], v[122:125], v[48:63]
	ds_read_b64_tr_b16 v[122:123], v78 offset:0x1400
	ds_read_b64_tr_b16 v[124:125], v78 offset:0x1c00
	v_mfma_f32_32x32x16_bf16 v[48:63], v[74:77], v[126:129], v[48:63]
	ds_read_b64_tr_b16 v[126:127], v78 offset:0x2400
	ds_read_b64_tr_b16 v[128:129], v78 offset:0x2c00
	v_mfma_f32_32x32x16_bf16 v[48:63], v[114:117], v[130:133], v[48:63]
	ds_read_b64_tr_b16 v[130:131], v78 offset:0x3400
	ds_read_b64_tr_b16 v[132:133], v78 offset:0x3c00
	s_waitcnt lgkmcnt(0)
	v_mfma_f32_32x32x16_bf16 v[32:47], v[66:69], v[118:121], v[32:47]
	ds_read_b64_tr_b16 v[118:119], v78 offset:0x600
	ds_read_b64_tr_b16 v[120:121], v78 offset:0xe00
	v_mfma_f32_32x32x16_bf16 v[32:47], v[70:73], v[122:125], v[32:47]
	ds_read_b64_tr_b16 v[122:123], v78 offset:0x1600
	ds_read_b64_tr_b16 v[124:125], v78 offset:0x1e00
	v_mfma_f32_32x32x16_bf16 v[32:47], v[74:77], v[126:129], v[32:47]
	ds_read_b64_tr_b16 v[126:127], v78 offset:0x2600
	ds_read_b64_tr_b16 v[128:129], v78 offset:0x2e00
	v_mfma_f32_32x32x16_bf16 v[32:47], v[114:117], v[130:133], v[32:47]
	ds_read_b64_tr_b16 v[130:131], v78 offset:0x3600
	ds_read_b64_tr_b16 v[132:133], v78 offset:0x3e00
	s_waitcnt lgkmcnt(0)
	v_mfma_f32_32x32x16_bf16 v[16:31], v[66:69], v[118:121], v[16:31]
	v_max_f32_e32 v66, v97, v97
	v_max_f32_e32 v67, v96, v96
	v_max_f32_e32 v66, v67, v66
	v_max3_f32 v66, v66, v98, v99
	v_max3_f32 v66, v66, v100, v101
	v_max3_f32 v66, v66, v102, v103
	v_max3_f32 v66, v66, v104, v105
	v_mfma_f32_32x32x16_bf16 v[16:31], v[70:73], v[122:125], v[16:31]
	v_max3_f32 v66, v66, v106, v107
	v_max3_f32 v66, v66, v108, v109
	v_max3_f32 v66, v66, v110, v111
	v_max3_f32 v66, v66, v80, v81
	v_max3_f32 v66, v66, v82, v83
	v_max3_f32 v66, v66, v84, v85
	v_max3_f32 v66, v66, v86, v87
	v_mfma_f32_32x32x16_bf16 v[16:31], v[74:77], v[126:129], v[16:31]
	v_max3_f32 v66, v66, v88, v89
	v_max3_f32 v66, v66, v90, v91
	v_max3_f32 v66, v66, v92, v93
	v_max3_f32 v66, v66, v94, v95
	v_mov_b32_e32 v67, v66
	s_nop 1
	v_permlane32_swap_b32_e32 v66, v67
	v_mfma_f32_32x32x16_bf16 v[16:31], v[114:117], v[130:133], v[16:31]
	v_max_f32_e32 v67, v67, v67
	v_max_f32_e32 v66, v66, v66
	v_max_f32_e32 v67, v66, v67
	v_cmp_eq_f32_e32 vcc, 0, v164
	v_cmp_ge_f32_e64 s[40:41], s75, v67
	s_and_b64 s[0:1], vcc, s[40:41]
	v_cndmask_b32_e64 v66, 0, 1, s[0:1]
	v_cmp_ne_u32_e32 vcc, 0, v66
	s_cmp_eq_u64 vcc, exec
	v_mov_b32_e32 v66, 1.0
	s_cbranch_scc0 .LBB0_815
	v_cmp_gt_f32_e32 vcc, 1.0, v66
	s_cbranch_vccz .LBB0_808
